# weight-transpose source loads marked non-temporal (read once)
# speedup vs baseline: 1.0184x; 1.0034x over previous
.LBB0_40:
	s_mul_hi_i32 s8, s83, 0x4fec04ff
	s_lshr_b32 s12, s8, 31
	s_ashr_i32 s8, s8, 13
	s_add_i32 s12, s8, s12
	s_mul_i32 s8, s12, 0xffff9980
	s_add_i32 s90, s83, s8
	s_ashr_i32 s13, s12, 31
	s_mul_i32 s14, s12, 0x1300000
	s_mul_hi_i32 s8, s12, 0x1300000
	s_waitcnt lgkmcnt(0)
	s_add_u32 s88, s10, s14
	s_addc_u32 s89, s11, s8
	s_cmpk_gt_i32 s90, 0xbf
	s_mov_b64 s[14:15], -1
	s_cbranch_scc0 .LBB0_62
	s_cmpk_gt_u32 s90, 0x3bf
	s_cbranch_scc0 .LBB0_59
	s_cmpk_gt_u32 s90, 0x47f
	s_cbranch_scc0 .LBB0_56
	s_cmpk_gt_u32 s90, 0x57f
	s_cbranch_scc0 .LBB0_53
	s_cmpk_gt_u32 s90, 0x67f
	s_cbranch_scc0 .LBB0_50
	s_cmpk_gt_u32 s90, 0x467f
	s_cbranch_scc0 .LBB0_47
	s_add_i32 s8, s90, 0xffffb980
	s_load_dwordx2 s[14:15], s[28:29], 0xc8
	s_lshr_b32 s8, s8, 9
	s_lshl_b64 s[44:45], s[12:13], 4
	s_add_u32 s44, s44, s8
	s_addc_u32 s45, s45, 0
	s_lshl_b64 s[92:93], s[44:45], 23
	s_waitcnt lgkmcnt(0)
	s_add_u32 s40, s14, s92
	s_addc_u32 s42, s15, s93
	s_lshl_b32 s8, s12, 8
	s_sub_i32 s8, s86, s8
	s_and_b32 s91, s85, 0x7c0
	s_and_b32 s8, s8, 0x3c0
	s_lshl_b64 s[14:15], s[44:45], 21
	s_add_u32 s44, s2, s14
	s_addc_u32 s45, s3, s15
	s_lshl_b32 s14, s8, 2
	s_add_u32 s14, s40, s14
	v_or_b32_e32 v52, s91, v9
	s_addc_u32 s15, s42, 0
	v_lshl_add_u64 v[10:11], s[14:15], 0, v[2:3]
	v_lshlrev_b32_e32 v52, 12, v52
	v_mov_b32_e32 v53, v3
	v_lshl_add_u64 v[10:11], v[10:11], 0, v[52:53]
	v_add_co_u32_e32 v56, vcc, s30, v10
	s_add_u32 s14, s44, s91
	s_nop 0
	v_addc_co_u32_e32 v57, vcc, 0, v11, vcc
	v_add_co_u32_e32 v60, vcc, s31, v10
	global_load_dwordx4 v[52:55], v[10:11], off nt
	s_nop 0
	global_load_dwordx4 v[56:59], v[56:57], off nt
	v_addc_co_u32_e32 v61, vcc, 0, v11, vcc
	v_add_co_u32_e32 v64, vcc, s33, v10
	s_addc_u32 s15, s45, 0
	s_nop 0
	v_addc_co_u32_e32 v65, vcc, 0, v11, vcc
	v_add_co_u32_e32 v68, vcc, s34, v10
	global_load_dwordx4 v[60:63], v[60:61], off nt
	s_nop 0
	global_load_dwordx4 v[64:67], v[64:65], off nt
	v_addc_co_u32_e32 v69, vcc, 0, v11, vcc
	v_add_co_u32_e32 v72, vcc, s35, v10
	s_nop 1
	v_addc_co_u32_e32 v73, vcc, 0, v11, vcc
	v_add_co_u32_e32 v76, vcc, s36, v10
	global_load_dwordx4 v[68:71], v[68:69], off nt
	s_nop 0
	global_load_dwordx4 v[72:75], v[72:73], off nt
	v_addc_co_u32_e32 v77, vcc, 0, v11, vcc
	v_add_co_u32_e32 v80, vcc, s37, v10
	s_nop 1
	v_addc_co_u32_e32 v81, vcc, 0, v11, vcc
	v_add_co_u32_e32 v84, vcc, s38, v10
	global_load_dwordx4 v[76:79], v[76:77], off nt
	s_nop 0
	global_load_dwordx4 v[80:83], v[80:81], off nt
	v_addc_co_u32_e32 v85, vcc, 0, v11, vcc
	v_add_co_u32_e32 v88, vcc, s39, v10
	s_nop 1
	v_addc_co_u32_e32 v89, vcc, 0, v11, vcc
	v_add_co_u32_e32 v92, vcc, s41, v10
	global_load_dwordx4 v[84:87], v[84:85], off nt
	s_nop 0
	global_load_dwordx4 v[88:91], v[88:89], off nt
	v_addc_co_u32_e32 v93, vcc, 0, v11, vcc
	v_add_co_u32_e32 v96, vcc, s43, v10
	s_nop 1
	v_addc_co_u32_e32 v97, vcc, 0, v11, vcc
	v_add_co_u32_e32 v100, vcc, s46, v10
	global_load_dwordx4 v[92:95], v[92:93], off nt
	s_nop 0
	global_load_dwordx4 v[96:99], v[96:97], off nt
	v_addc_co_u32_e32 v101, vcc, 0, v11, vcc
	v_add_co_u32_e32 v104, vcc, s47, v10
	s_nop 1
	v_addc_co_u32_e32 v105, vcc, 0, v11, vcc
	v_add_co_u32_e32 v108, vcc, s48, v10
	global_load_dwordx4 v[100:103], v[100:101], off nt
	s_nop 0
	global_load_dwordx4 v[104:107], v[104:105], off nt
	v_addc_co_u32_e32 v109, vcc, 0, v11, vcc
	v_add_co_u32_e32 v10, vcc, s49, v10
	s_nop 1
	v_addc_co_u32_e32 v11, vcc, 0, v11, vcc
	global_load_dwordx4 v[108:111], v[108:109], off nt
	s_nop 0
	global_load_dwordx4 v[112:115], v[10:11], off nt
	v_lshl_add_u64 v[10:11], s[14:15], 0, v[4:5]
	s_mov_b64 s[14:15], 0
	s_waitcnt vmcnt(14)
	ds_write2_b32 v12, v52, v56 offset1:4
	ds_write2_b32 v12, v53, v57 offset0:65 offset1:69
	ds_write2_b32 v12, v54, v58 offset0:130 offset1:134
	ds_write2_b32 v12, v55, v59 offset0:195 offset1:199
	s_waitcnt vmcnt(12)
	ds_write2_b32 v12, v60, v64 offset0:8 offset1:12
	ds_write2_b32 v12, v61, v65 offset0:73 offset1:77
	ds_write2_b32 v12, v62, v66 offset0:138 offset1:142
	ds_write2_b32 v12, v63, v67 offset0:203 offset1:207
	s_waitcnt vmcnt(10)
	ds_write2_b32 v12, v68, v72 offset0:16 offset1:20
	ds_write2_b32 v12, v69, v73 offset0:81 offset1:85
	ds_write2_b32 v12, v70, v74 offset0:146 offset1:150
	ds_write2_b32 v12, v71, v75 offset0:211 offset1:215
	s_waitcnt vmcnt(8)
	ds_write2_b32 v12, v76, v80 offset0:24 offset1:28
	ds_write2_b32 v12, v77, v81 offset0:89 offset1:93
	ds_write2_b32 v12, v78, v82 offset0:154 offset1:158
	ds_write2_b32 v12, v79, v83 offset0:219 offset1:223
	s_waitcnt vmcnt(6)
	ds_write2_b32 v12, v84, v88 offset0:32 offset1:36
	ds_write2_b32 v12, v85, v89 offset0:97 offset1:101
	ds_write2_b32 v12, v86, v90 offset0:162 offset1:166
	ds_write2_b32 v12, v87, v91 offset0:227 offset1:231
	s_waitcnt vmcnt(4)
	ds_write2_b32 v12, v92, v96 offset0:40 offset1:44
	ds_write2_b32 v12, v93, v97 offset0:105 offset1:109
	ds_write2_b32 v12, v94, v98 offset0:170 offset1:174
	ds_write2_b32 v12, v95, v99 offset0:235 offset1:239
	s_waitcnt vmcnt(2)
	ds_write2_b32 v12, v100, v104 offset0:48 offset1:52
	ds_write2_b32 v12, v101, v105 offset0:113 offset1:117
	ds_write2_b32 v12, v102, v106 offset0:178 offset1:182
	ds_write2_b32 v12, v103, v107 offset0:243 offset1:247
	s_waitcnt vmcnt(0)
	ds_write2_b32 v12, v108, v112 offset0:56 offset1:60
	ds_write2_b32 v12, v109, v113 offset0:121 offset1:125
	ds_write2_b32 v12, v110, v114 offset0:186 offset1:190
	ds_write2_b32 v12, v111, v115 offset0:251 offset1:255
	s_waitcnt lgkmcnt(0)
	ds_read2_b32 v[52:53], v14 offset1:1
	ds_read2_b32 v[54:55], v14 offset0:2 offset1:3
	ds_read2_b32 v[56:57], v14 offset0:4 offset1:5
	ds_read2_b32 v[58:59], v14 offset0:6 offset1:7
	s_waitcnt lgkmcnt(2)
	v_mul_f32_e32 v54, 0x42800000, v54
	v_mul_f32_e32 v52, 0x42800000, v52
	v_mul_f32_e32 v53, 0x42800000, v53
	v_med3_f32 v60, v52, s50, v51
	v_med3_f32 v53, v53, s50, v51
	v_mov_b32_e32 v52, v3
	v_cvt_pk_fp8_f32 v52, v60, v53
	v_mul_f32_e32 v53, 0x42800000, v55
	v_med3_f32 v54, v54, s50, v51
	v_med3_f32 v53, v53, s50, v51
	v_cvt_pk_fp8_f32 v52, v54, v53 op_sel:[0,0,1]
	s_waitcnt lgkmcnt(1)
	v_mul_f32_e32 v53, 0x42800000, v56
	v_mul_f32_e32 v54, 0x42800000, v57
	v_med3_f32 v56, v53, s50, v51
	v_med3_f32 v54, v54, s50, v51
	v_mov_b32_e32 v53, v3
	v_cvt_pk_fp8_f32 v53, v56, v54
	s_waitcnt lgkmcnt(0)
	v_mul_f32_e32 v55, 0x42800000, v58
	v_mul_f32_e32 v54, 0x42800000, v59
	v_med3_f32 v55, v55, s50, v51
	v_med3_f32 v54, v54, s50, v51
	v_cvt_pk_fp8_f32 v53, v55, v54 op_sel:[0,0,1]
	v_or_b32_e32 v54, s8, v13
	v_lshlrev_b32_e32 v54, 11, v54
	v_mov_b32_e32 v55, v3
	ds_read2_b32 v[56:57], v26 offset1:1
	v_lshl_add_u64 v[54:55], v[10:11], 0, v[54:55]
	global_store_dwordx2 v[54:55], v[52:53], off
	ds_read2_b32 v[52:53], v26 offset0:2 offset1:3
	ds_read2_b32 v[54:55], v26 offset0:4 offset1:5
	ds_read2_b32 v[58:59], v26 offset0:6 offset1:7
	s_waitcnt lgkmcnt(3)
	v_mul_f32_e32 v56, 0x42800000, v56
	v_mul_f32_e32 v57, 0x42800000, v57
	s_waitcnt lgkmcnt(2)
	v_mul_f32_e32 v60, 0x42800000, v52
	v_med3_f32 v56, v56, s50, v51
	v_med3_f32 v57, v57, s50, v51
	v_mov_b32_e32 v52, v3
	v_cvt_pk_fp8_f32 v52, v56, v57
	v_mul_f32_e32 v53, 0x42800000, v53
	v_med3_f32 v56, v60, s50, v51
	v_med3_f32 v53, v53, s50, v51
	v_cvt_pk_fp8_f32 v52, v56, v53 op_sel:[0,0,1]
	s_waitcnt lgkmcnt(1)
	v_mul_f32_e32 v53, 0x42800000, v54
	v_mul_f32_e32 v54, 0x42800000, v55
	v_med3_f32 v56, v53, s50, v51
	v_med3_f32 v54, v54, s50, v51
	v_mov_b32_e32 v53, v3
	v_cvt_pk_fp8_f32 v53, v56, v54
	s_waitcnt lgkmcnt(0)
	v_mul_f32_e32 v55, 0x42800000, v58
	v_mul_f32_e32 v54, 0x42800000, v59
	v_med3_f32 v55, v55, s50, v51
	v_med3_f32 v54, v54, s50, v51
	v_cvt_pk_fp8_f32 v53, v55, v54 op_sel:[0,0,1]
	v_or_b32_e32 v54, s8, v15
	v_lshlrev_b32_e32 v54, 11, v54
	v_mov_b32_e32 v55, v3
	ds_read2_b32 v[56:57], v27 offset1:1
	v_lshl_add_u64 v[54:55], v[10:11], 0, v[54:55]
	global_store_dwordx2 v[54:55], v[52:53], off
	ds_read2_b32 v[52:53], v28 offset1:1
	ds_read2_b32 v[54:55], v29 offset1:1
	ds_read2_b32 v[58:59], v30 offset1:1
	s_waitcnt lgkmcnt(3)
	v_mul_f32_e32 v56, 0x42800000, v56
	v_mul_f32_e32 v57, 0x42800000, v57
	s_waitcnt lgkmcnt(2)
	v_mul_f32_e32 v60, 0x42800000, v52
	v_med3_f32 v56, v56, s50, v51
	v_med3_f32 v57, v57, s50, v51
	v_mov_b32_e32 v52, v3
	v_cvt_pk_fp8_f32 v52, v56, v57
	v_mul_f32_e32 v53, 0x42800000, v53
	v_med3_f32 v56, v60, s50, v51
	v_med3_f32 v53, v53, s50, v51
	v_cvt_pk_fp8_f32 v52, v56, v53 op_sel:[0,0,1]
	s_waitcnt lgkmcnt(1)
	v_mul_f32_e32 v53, 0x42800000, v54
	v_mul_f32_e32 v54, 0x42800000, v55
	v_med3_f32 v56, v53, s50, v51
	v_med3_f32 v54, v54, s50, v51
	v_mov_b32_e32 v53, v3
	v_cvt_pk_fp8_f32 v53, v56, v54
	s_waitcnt lgkmcnt(0)
	v_mul_f32_e32 v55, 0x42800000, v58
	v_mul_f32_e32 v54, 0x42800000, v59
	v_med3_f32 v55, v55, s50, v51
	v_med3_f32 v54, v54, s50, v51
	v_cvt_pk_fp8_f32 v53, v55, v54 op_sel:[0,0,1]
	v_or_b32_e32 v54, s8, v16
	v_lshlrev_b32_e32 v54, 11, v54
	v_mov_b32_e32 v55, v3
	ds_read2_b32 v[56:57], v31 offset1:1
	v_lshl_add_u64 v[54:55], v[10:11], 0, v[54:55]
	global_store_dwordx2 v[54:55], v[52:53], off
	ds_read2_b32 v[52:53], v32 offset1:1
	ds_read2_b32 v[54:55], v33 offset1:1
	ds_read2_b32 v[58:59], v34 offset1:1
	s_waitcnt lgkmcnt(3)
	v_mul_f32_e32 v56, 0x42800000, v56
	v_mul_f32_e32 v57, 0x42800000, v57
	s_waitcnt lgkmcnt(2)
	v_mul_f32_e32 v60, 0x42800000, v52
	v_med3_f32 v56, v56, s50, v51
	v_med3_f32 v57, v57, s50, v51
	v_mov_b32_e32 v52, v3
	v_cvt_pk_fp8_f32 v52, v56, v57
	v_mul_f32_e32 v53, 0x42800000, v53
	v_med3_f32 v56, v60, s50, v51
	v_med3_f32 v53, v53, s50, v51
	v_cvt_pk_fp8_f32 v52, v56, v53 op_sel:[0,0,1]
	s_waitcnt lgkmcnt(1)
	v_mul_f32_e32 v53, 0x42800000, v54
	v_mul_f32_e32 v54, 0x42800000, v55
	v_med3_f32 v56, v53, s50, v51
	v_med3_f32 v54, v54, s50, v51
	v_mov_b32_e32 v53, v3
	v_cvt_pk_fp8_f32 v53, v56, v54
	s_waitcnt lgkmcnt(0)
	v_mul_f32_e32 v55, 0x42800000, v58
	v_mul_f32_e32 v54, 0x42800000, v59
	v_med3_f32 v55, v55, s50, v51
	v_med3_f32 v54, v54, s50, v51
	v_cvt_pk_fp8_f32 v53, v55, v54 op_sel:[0,0,1]
	v_or_b32_e32 v54, s8, v17
	v_lshlrev_b32_e32 v54, 11, v54
	v_mov_b32_e32 v55, v3
	ds_read2_b32 v[56:57], v35 offset1:1
	v_lshl_add_u64 v[54:55], v[10:11], 0, v[54:55]
	global_store_dwordx2 v[54:55], v[52:53], off
	ds_read2_b32 v[52:53], v36 offset1:1
	ds_read2_b32 v[54:55], v37 offset1:1
	ds_read2_b32 v[58:59], v38 offset1:1
	s_waitcnt lgkmcnt(3)
	v_mul_f32_e32 v56, 0x42800000, v56
	v_mul_f32_e32 v57, 0x42800000, v57
	s_waitcnt lgkmcnt(2)
	v_mul_f32_e32 v60, 0x42800000, v52
	v_med3_f32 v56, v56, s50, v51
	v_med3_f32 v57, v57, s50, v51
	v_mov_b32_e32 v52, v3
	v_cvt_pk_fp8_f32 v52, v56, v57
	v_mul_f32_e32 v53, 0x42800000, v53
	v_med3_f32 v56, v60, s50, v51
	v_med3_f32 v53, v53, s50, v51
	v_cvt_pk_fp8_f32 v52, v56, v53 op_sel:[0,0,1]
	s_waitcnt lgkmcnt(1)
	v_mul_f32_e32 v53, 0x42800000, v54
	v_mul_f32_e32 v54, 0x42800000, v55
	v_med3_f32 v56, v53, s50, v51
	v_med3_f32 v54, v54, s50, v51
	v_mov_b32_e32 v53, v3
	v_cvt_pk_fp8_f32 v53, v56, v54
	s_waitcnt lgkmcnt(0)
	v_mul_f32_e32 v55, 0x42800000, v58
	v_mul_f32_e32 v54, 0x42800000, v59
	v_med3_f32 v55, v55, s50, v51
	v_med3_f32 v54, v54, s50, v51
	v_cvt_pk_fp8_f32 v53, v55, v54 op_sel:[0,0,1]
	v_or_b32_e32 v54, s8, v18
	v_lshlrev_b32_e32 v54, 11, v54
	v_mov_b32_e32 v55, v3
	ds_read2_b32 v[56:57], v39 offset1:1
	v_lshl_add_u64 v[54:55], v[10:11], 0, v[54:55]
	global_store_dwordx2 v[54:55], v[52:53], off
	ds_read2_b32 v[52:53], v40 offset1:1
	ds_read2_b32 v[54:55], v41 offset1:1
	ds_read2_b32 v[58:59], v42 offset1:1
	s_waitcnt lgkmcnt(3)
	v_mul_f32_e32 v56, 0x42800000, v56
	v_mul_f32_e32 v57, 0x42800000, v57
	s_waitcnt lgkmcnt(2)
	v_mul_f32_e32 v60, 0x42800000, v52
	v_med3_f32 v56, v56, s50, v51
	v_med3_f32 v57, v57, s50, v51
	v_mov_b32_e32 v52, v3
	v_cvt_pk_fp8_f32 v52, v56, v57
	v_mul_f32_e32 v53, 0x42800000, v53
	v_med3_f32 v56, v60, s50, v51
	v_med3_f32 v53, v53, s50, v51
	v_cvt_pk_fp8_f32 v52, v56, v53 op_sel:[0,0,1]
	s_waitcnt lgkmcnt(1)
	v_mul_f32_e32 v53, 0x42800000, v54
	v_mul_f32_e32 v54, 0x42800000, v55
	v_med3_f32 v56, v53, s50, v51
	v_med3_f32 v54, v54, s50, v51
	v_mov_b32_e32 v53, v3
	v_cvt_pk_fp8_f32 v53, v56, v54
	s_waitcnt lgkmcnt(0)
	v_mul_f32_e32 v55, 0x42800000, v58
	v_mul_f32_e32 v54, 0x42800000, v59
	v_med3_f32 v55, v55, s50, v51
	v_med3_f32 v54, v54, s50, v51
	v_cvt_pk_fp8_f32 v53, v55, v54 op_sel:[0,0,1]
	v_or_b32_e32 v54, s8, v19
	v_lshlrev_b32_e32 v54, 11, v54
	v_mov_b32_e32 v55, v3
	ds_read2_b32 v[56:57], v43 offset1:1
	v_lshl_add_u64 v[54:55], v[10:11], 0, v[54:55]
	global_store_dwordx2 v[54:55], v[52:53], off
	ds_read2_b32 v[52:53], v44 offset1:1
	ds_read2_b32 v[54:55], v45 offset1:1
	ds_read2_b32 v[58:59], v46 offset1:1
	s_waitcnt lgkmcnt(3)
	v_mul_f32_e32 v56, 0x42800000, v56
	v_mul_f32_e32 v57, 0x42800000, v57
	s_waitcnt lgkmcnt(2)
	v_mul_f32_e32 v60, 0x42800000, v52
	v_med3_f32 v56, v56, s50, v51
	v_med3_f32 v57, v57, s50, v51
	v_mov_b32_e32 v52, v3
	v_cvt_pk_fp8_f32 v52, v56, v57
	v_mul_f32_e32 v53, 0x42800000, v53
	v_med3_f32 v56, v60, s50, v51
	v_med3_f32 v53, v53, s50, v51
	v_cvt_pk_fp8_f32 v52, v56, v53 op_sel:[0,0,1]
	s_waitcnt lgkmcnt(1)
	v_mul_f32_e32 v53, 0x42800000, v54
	v_mul_f32_e32 v54, 0x42800000, v55
	v_med3_f32 v56, v53, s50, v51
	v_med3_f32 v54, v54, s50, v51
	v_mov_b32_e32 v53, v3
	v_cvt_pk_fp8_f32 v53, v56, v54
	s_waitcnt lgkmcnt(0)
	v_mul_f32_e32 v55, 0x42800000, v58
	v_mul_f32_e32 v54, 0x42800000, v59
	v_med3_f32 v55, v55, s50, v51
	v_med3_f32 v54, v54, s50, v51
	v_cvt_pk_fp8_f32 v53, v55, v54 op_sel:[0,0,1]
	v_or_b32_e32 v54, s8, v20
	v_lshlrev_b32_e32 v54, 11, v54
	v_mov_b32_e32 v55, v3
	ds_read2_b32 v[56:57], v47 offset1:1
	v_lshl_add_u64 v[54:55], v[10:11], 0, v[54:55]
	global_store_dwordx2 v[54:55], v[52:53], off
	ds_read2_b32 v[52:53], v48 offset1:1
	ds_read2_b32 v[54:55], v49 offset1:1
	ds_read2_b32 v[58:59], v50 offset1:1
	s_waitcnt lgkmcnt(3)
	v_mul_f32_e32 v56, 0x42800000, v56
	v_mul_f32_e32 v57, 0x42800000, v57
	s_waitcnt lgkmcnt(2)
	v_mul_f32_e32 v60, 0x42800000, v52
	v_med3_f32 v56, v56, s50, v51
	v_med3_f32 v57, v57, s50, v51
	v_mov_b32_e32 v52, v3
	v_cvt_pk_fp8_f32 v52, v56, v57
	v_mul_f32_e32 v53, 0x42800000, v53
	v_med3_f32 v56, v60, s50, v51
	v_med3_f32 v53, v53, s50, v51
	v_cvt_pk_fp8_f32 v52, v56, v53 op_sel:[0,0,1]
	s_waitcnt lgkmcnt(1)
	v_mul_f32_e32 v53, 0x42800000, v54
	v_mul_f32_e32 v54, 0x42800000, v55
	v_med3_f32 v56, v53, s50, v51
	v_med3_f32 v54, v54, s50, v51
	v_mov_b32_e32 v53, v3
	v_cvt_pk_fp8_f32 v53, v56, v54
	s_waitcnt lgkmcnt(0)
	v_mul_f32_e32 v55, 0x42800000, v58
	v_mul_f32_e32 v54, 0x42800000, v59
	v_med3_f32 v55, v55, s50, v51
	v_med3_f32 v54, v54, s50, v51
	v_cvt_pk_fp8_f32 v53, v55, v54 op_sel:[0,0,1]
	v_or_b32_e32 v54, s8, v21
	v_lshlrev_b32_e32 v54, 11, v54
	v_mov_b32_e32 v55, v3
	v_lshl_add_u64 v[10:11], v[10:11], 0, v[54:55]
	global_store_dwordx2 v[10:11], v[52:53], off
	s_waitcnt lgkmcnt(0)
.LBB0_47:
	s_andn2_b64 vcc, exec, s[14:15]
	s_cbranch_vccnz .LBB0_49
	s_add_i32 s8, s90, 0xfffff980
	s_bfe_u32 s40, s8, 0x40009
	s_bfe_u32 s42, s8, 0x50004
	s_cmpk_lt_u32 s8, 0x2000
	s_movk_i32 s14, 0xb8
	s_cselect_b32 s14, s14, 0xc0
	s_add_u32 s14, s28, s14
	s_addc_u32 s15, s29, 0
	s_load_dwordx2 s[14:15], s[14:15], 0x0
	s_lshl_b64 s[44:45], s[12:13], 4
	s_or_b32 s44, s44, s40
	s_lshl_b64 s[92:93], s[44:45], 23
	v_mov_b32_e32 v53, v3
	s_waitcnt lgkmcnt(0)
	s_add_u32 s40, s14, s92
	s_addc_u32 s91, s15, s93
	s_lshl_b64 s[14:15], s[44:45], 22
	s_add_u32 s44, s16, s14
	s_addc_u32 s45, s17, s15
	s_lshr_b32 s8, s8, 10
	s_lshl_b32 s14, s42, 7
	s_and_b32 s8, s8, 0x3ffff8
	s_and_b32 s92, s85, 0x3c0
	s_add_i32 s8, s14, s8
	s_lshl_b32 s14, s42, 8
	s_add_u32 s14, s40, s14
	v_or_b32_e32 v52, s92, v9
	s_addc_u32 s15, s91, 0
	v_lshl_add_u64 v[10:11], s[14:15], 0, v[2:3]
	v_lshlrev_b32_e32 v52, 13, v52
	v_lshl_add_u64 v[10:11], v[10:11], 0, v[52:53]
	v_add_co_u32_e32 v56, vcc, s31, v10
	s_mov_b32 s14, 0x40000
	s_nop 0
	v_addc_co_u32_e32 v57, vcc, 0, v11, vcc
	v_add_co_u32_e32 v60, vcc, s34, v10
	global_load_dwordx4 v[52:55], v[10:11], off nt
	s_nop 0
	global_load_dwordx4 v[56:59], v[56:57], off nt
	v_addc_co_u32_e32 v61, vcc, 0, v11, vcc
	v_add_co_u32_e32 v64, vcc, s36, v10
	s_nop 1
	v_addc_co_u32_e32 v65, vcc, 0, v11, vcc
	v_add_co_u32_e32 v68, vcc, s38, v10
	global_load_dwordx4 v[60:63], v[60:61], off nt
	s_nop 0
	global_load_dwordx4 v[64:67], v[64:65], off nt
	v_addc_co_u32_e32 v69, vcc, 0, v11, vcc
	v_add_co_u32_e32 v72, vcc, s41, v10
	s_nop 1
	v_addc_co_u32_e32 v73, vcc, 0, v11, vcc
	v_add_co_u32_e32 v76, vcc, s46, v10
	global_load_dwordx4 v[68:71], v[68:69], off nt
	s_nop 0
	global_load_dwordx4 v[72:75], v[72:73], off nt
	v_addc_co_u32_e32 v77, vcc, 0, v11, vcc
	v_add_co_u32_e32 v80, vcc, s48, v10
	s_nop 1
	v_addc_co_u32_e32 v81, vcc, 0, v11, vcc
	v_add_co_u32_e32 v84, vcc, s14, v10
	s_mov_b32 s14, 0x48000
	s_nop 0
	v_addc_co_u32_e32 v85, vcc, 0, v11, vcc
	v_add_co_u32_e32 v88, vcc, s14, v10
	s_mov_b32 s14, 0x50000
	s_nop 0
	v_addc_co_u32_e32 v89, vcc, 0, v11, vcc
	v_add_co_u32_e32 v92, vcc, s14, v10
	s_mov_b32 s14, 0x58000
	s_nop 0
	v_addc_co_u32_e32 v93, vcc, 0, v11, vcc
	v_add_co_u32_e32 v96, vcc, s14, v10
	s_mov_b32 s14, 0x68000
	s_nop 0
	v_addc_co_u32_e32 v97, vcc, 0, v11, vcc
	v_add_co_u32_e32 v100, vcc, s51, v10
	global_load_dwordx4 v[76:79], v[76:77], off nt
	s_nop 0
	global_load_dwordx4 v[80:83], v[80:81], off nt
	v_addc_co_u32_e32 v101, vcc, 0, v11, vcc
	v_add_co_u32_e32 v104, vcc, s14, v10
	s_mov_b32 s14, 0x70000
	s_nop 0
	v_addc_co_u32_e32 v105, vcc, 0, v11, vcc
	v_add_co_u32_e32 v108, vcc, s14, v10
	s_mov_b32 s14, 0x78000
	s_nop 0
	v_addc_co_u32_e32 v109, vcc, 0, v11, vcc
	v_add_co_u32_e32 v10, vcc, s14, v10
	global_load_dwordx4 v[84:87], v[84:85], off nt
	s_nop 0
	global_load_dwordx4 v[88:91], v[88:89], off nt
	s_nop 0
	global_load_dwordx4 v[92:95], v[92:93], off nt
	s_nop 0
	global_load_dwordx4 v[96:99], v[96:97], off nt
	s_nop 0
	global_load_dwordx4 v[100:103], v[100:101], off nt
	s_nop 0
	global_load_dwordx4 v[104:107], v[104:105], off nt
	v_addc_co_u32_e32 v11, vcc, 0, v11, vcc
	global_load_dwordx4 v[108:111], v[108:109], off nt
	s_nop 0
	global_load_dwordx4 v[112:115], v[10:11], off nt
	s_add_u32 s14, s44, s92
	s_addc_u32 s15, s45, 0
	v_lshl_add_u64 v[10:11], s[14:15], 0, v[4:5]
	s_waitcnt vmcnt(14)
	ds_write2_b32 v12, v52, v56 offset1:4
	ds_write2_b32 v12, v53, v57 offset0:65 offset1:69
	ds_write2_b32 v12, v54, v58 offset0:130 offset1:134
	ds_write2_b32 v12, v55, v59 offset0:195 offset1:199
	s_waitcnt vmcnt(12)
	ds_write2_b32 v12, v60, v64 offset0:8 offset1:12
	ds_write2_b32 v12, v61, v65 offset0:73 offset1:77
	ds_write2_b32 v12, v62, v66 offset0:138 offset1:142
	ds_write2_b32 v12, v63, v67 offset0:203 offset1:207
	s_waitcnt vmcnt(10)
	ds_write2_b32 v12, v68, v72 offset0:16 offset1:20
	ds_write2_b32 v12, v69, v73 offset0:81 offset1:85
	ds_write2_b32 v12, v70, v74 offset0:146 offset1:150
	ds_write2_b32 v12, v71, v75 offset0:211 offset1:215
	s_waitcnt vmcnt(8)
	ds_write2_b32 v12, v76, v80 offset0:24 offset1:28
	ds_write2_b32 v12, v77, v81 offset0:89 offset1:93
	ds_write2_b32 v12, v78, v82 offset0:154 offset1:158
	ds_write2_b32 v12, v79, v83 offset0:219 offset1:223
	s_waitcnt vmcnt(6)
	ds_write2_b32 v12, v84, v88 offset0:32 offset1:36
	ds_write2_b32 v12, v85, v89 offset0:97 offset1:101
	ds_write2_b32 v12, v86, v90 offset0:162 offset1:166
	ds_write2_b32 v12, v87, v91 offset0:227 offset1:231
	s_waitcnt vmcnt(4)
	ds_write2_b32 v12, v92, v96 offset0:40 offset1:44
	ds_write2_b32 v12, v93, v97 offset0:105 offset1:109
	ds_write2_b32 v12, v94, v98 offset0:170 offset1:174
	ds_write2_b32 v12, v95, v99 offset0:235 offset1:239
	s_waitcnt vmcnt(2)
	ds_write2_b32 v12, v100, v104 offset0:48 offset1:52
	ds_write2_b32 v12, v101, v105 offset0:113 offset1:117
	ds_write2_b32 v12, v102, v106 offset0:178 offset1:182
	ds_write2_b32 v12, v103, v107 offset0:243 offset1:247
	s_waitcnt vmcnt(0)
	ds_write2_b32 v12, v108, v112 offset0:56 offset1:60
	ds_write2_b32 v12, v109, v113 offset0:121 offset1:125
	ds_write2_b32 v12, v110, v114 offset0:186 offset1:190
	ds_write2_b32 v12, v111, v115 offset0:251 offset1:255
	s_waitcnt lgkmcnt(0)
	ds_read2_b32 v[52:53], v14 offset1:1
	ds_read2_b32 v[54:55], v14 offset0:2 offset1:3
	ds_read2_b32 v[56:57], v14 offset0:4 offset1:5
	ds_read2_b32 v[58:59], v14 offset0:6 offset1:7
	s_waitcnt lgkmcnt(2)
	v_mul_f32_e32 v54, 0x42800000, v54
	v_mul_f32_e32 v52, 0x42800000, v52
	v_mul_f32_e32 v53, 0x42800000, v53
	v_med3_f32 v60, v52, s50, v51
	v_med3_f32 v53, v53, s50, v51
	v_mov_b32_e32 v52, v3
	v_cvt_pk_fp8_f32 v52, v60, v53
	v_mul_f32_e32 v53, 0x42800000, v55
	v_med3_f32 v54, v54, s50, v51
	v_med3_f32 v53, v53, s50, v51
	v_cvt_pk_fp8_f32 v52, v54, v53 op_sel:[0,0,1]
	s_waitcnt lgkmcnt(1)
	v_mul_f32_e32 v53, 0x42800000, v56
	v_mul_f32_e32 v54, 0x42800000, v57
	v_med3_f32 v56, v53, s50, v51
	v_med3_f32 v54, v54, s50, v51
	v_mov_b32_e32 v53, v3
	v_cvt_pk_fp8_f32 v53, v56, v54
	s_waitcnt lgkmcnt(0)
	v_mul_f32_e32 v55, 0x42800000, v58
	v_mul_f32_e32 v54, 0x42800000, v59
	v_med3_f32 v55, v55, s50, v51
	v_med3_f32 v54, v54, s50, v51
	v_cvt_pk_fp8_f32 v53, v55, v54 op_sel:[0,0,1]
	v_or_b32_e32 v54, s8, v13
	v_mov_b32_e32 v55, v3
	v_lshlrev_b64 v[54:55], 10, v[54:55]
	v_lshl_add_u64 v[54:55], v[10:11], 0, v[54:55]
	global_store_dwordx2 v[54:55], v[52:53], off
	v_add_u32_e32 v52, 0x820, v14
	ds_read2_b32 v[52:53], v52 offset1:1
	v_add_u32_e32 v54, 0x828, v14
	v_add_u32_e32 v56, 0x830, v14
	v_add_u32_e32 v58, 0x838, v14
	ds_read2_b32 v[54:55], v54 offset1:1
	ds_read2_b32 v[56:57], v56 offset1:1
	ds_read2_b32 v[58:59], v58 offset1:1
	s_waitcnt lgkmcnt(3)
	v_mul_f32_e32 v52, 0x42800000, v52
	v_mul_f32_e32 v53, 0x42800000, v53
	v_med3_f32 v60, v52, s50, v51
	v_med3_f32 v53, v53, s50, v51
	v_mov_b32_e32 v52, v3
	v_cvt_pk_fp8_f32 v52, v60, v53
	s_waitcnt lgkmcnt(2)
	v_mul_f32_e32 v54, 0x42800000, v54
	v_mul_f32_e32 v53, 0x42800000, v55
	v_med3_f32 v54, v54, s50, v51
	v_med3_f32 v53, v53, s50, v51
	v_cvt_pk_fp8_f32 v52, v54, v53 op_sel:[0,0,1]
	s_waitcnt lgkmcnt(1)
	v_mul_f32_e32 v53, 0x42800000, v56
	v_mul_f32_e32 v54, 0x42800000, v57
	v_med3_f32 v56, v53, s50, v51
	v_med3_f32 v54, v54, s50, v51
	v_mov_b32_e32 v53, v3
	v_cvt_pk_fp8_f32 v53, v56, v54
	s_waitcnt lgkmcnt(0)
	v_mul_f32_e32 v55, 0x42800000, v58
	v_mul_f32_e32 v54, 0x42800000, v59
	v_med3_f32 v55, v55, s50, v51
	v_med3_f32 v54, v54, s50, v51
	v_cvt_pk_fp8_f32 v53, v55, v54 op_sel:[0,0,1]
	v_add_u32_e32 v54, s8, v16
	v_mov_b32_e32 v55, v3
	v_lshlrev_b64 v[54:55], 10, v[54:55]
	ds_read2_b32 v[56:57], v27 offset1:1
	v_lshl_add_u64 v[54:55], v[10:11], 0, v[54:55]
	global_store_dwordx2 v[54:55], v[52:53], off
	ds_read2_b32 v[52:53], v28 offset1:1
	ds_read2_b32 v[54:55], v29 offset1:1
	ds_read2_b32 v[58:59], v30 offset1:1
	s_waitcnt lgkmcnt(3)
	v_mul_f32_e32 v56, 0x42800000, v56
	v_mul_f32_e32 v57, 0x42800000, v57
	s_waitcnt lgkmcnt(2)
	v_mul_f32_e32 v60, 0x42800000, v52
	v_med3_f32 v56, v56, s50, v51
	v_med3_f32 v57, v57, s50, v51
	v_mov_b32_e32 v52, v3
	v_cvt_pk_fp8_f32 v52, v56, v57
	v_mul_f32_e32 v53, 0x42800000, v53
	v_med3_f32 v56, v60, s50, v51
	v_med3_f32 v53, v53, s50, v51
	v_cvt_pk_fp8_f32 v52, v56, v53 op_sel:[0,0,1]
	s_waitcnt lgkmcnt(1)
	v_mul_f32_e32 v53, 0x42800000, v54
	v_mul_f32_e32 v54, 0x42800000, v55
	v_med3_f32 v56, v53, s50, v51
	v_med3_f32 v54, v54, s50, v51
	v_mov_b32_e32 v53, v3
	v_cvt_pk_fp8_f32 v53, v56, v54
	s_waitcnt lgkmcnt(0)
	v_mul_f32_e32 v55, 0x42800000, v58
	v_mul_f32_e32 v54, 0x42800000, v59
	v_med3_f32 v55, v55, s50, v51
	v_med3_f32 v54, v54, s50, v51
	v_cvt_pk_fp8_f32 v53, v55, v54 op_sel:[0,0,1]
	v_add_u32_e32 v54, s8, v18
	v_mov_b32_e32 v55, v3
	v_lshlrev_b64 v[54:55], 10, v[54:55]
	v_lshl_add_u64 v[54:55], v[10:11], 0, v[54:55]
	global_store_dwordx2 v[54:55], v[52:53], off
	v_add_u32_e32 v52, 0x1860, v14
	ds_read2_b32 v[52:53], v52 offset1:1
	v_add_u32_e32 v54, 0x1868, v14
	v_add_u32_e32 v56, 0x1870, v14
	v_add_u32_e32 v58, 0x1878, v14
	ds_read2_b32 v[54:55], v54 offset1:1
	ds_read2_b32 v[56:57], v56 offset1:1
	ds_read2_b32 v[58:59], v58 offset1:1
	s_waitcnt lgkmcnt(3)
	v_mul_f32_e32 v52, 0x42800000, v52
	v_mul_f32_e32 v53, 0x42800000, v53
	v_med3_f32 v60, v52, s50, v51
	v_med3_f32 v53, v53, s50, v51
	v_mov_b32_e32 v52, v3
	v_cvt_pk_fp8_f32 v52, v60, v53
	s_waitcnt lgkmcnt(2)
	v_mul_f32_e32 v54, 0x42800000, v54
	v_mul_f32_e32 v53, 0x42800000, v55
	v_med3_f32 v54, v54, s50, v51
	v_med3_f32 v53, v53, s50, v51
	v_cvt_pk_fp8_f32 v52, v54, v53 op_sel:[0,0,1]
	s_waitcnt lgkmcnt(1)
	v_mul_f32_e32 v53, 0x42800000, v56
	v_mul_f32_e32 v54, 0x42800000, v57
	v_med3_f32 v56, v53, s50, v51
	v_med3_f32 v54, v54, s50, v51
	v_mov_b32_e32 v53, v3
	v_cvt_pk_fp8_f32 v53, v56, v54
	s_waitcnt lgkmcnt(0)
	v_mul_f32_e32 v55, 0x42800000, v58
	v_mul_f32_e32 v54, 0x42800000, v59
	v_med3_f32 v55, v55, s50, v51
	v_med3_f32 v54, v54, s50, v51
	v_cvt_pk_fp8_f32 v53, v55, v54 op_sel:[0,0,1]
	v_add_u32_e32 v54, s8, v20
	v_mov_b32_e32 v55, v3
	v_lshlrev_b64 v[54:55], 10, v[54:55]
	ds_read2_b32 v[56:57], v35 offset1:1
	v_lshl_add_u64 v[54:55], v[10:11], 0, v[54:55]
	global_store_dwordx2 v[54:55], v[52:53], off
	ds_read2_b32 v[52:53], v36 offset1:1
	ds_read2_b32 v[54:55], v37 offset1:1
	ds_read2_b32 v[58:59], v38 offset1:1
	s_waitcnt lgkmcnt(3)
	v_mul_f32_e32 v56, 0x42800000, v56
	v_mul_f32_e32 v57, 0x42800000, v57
	s_waitcnt lgkmcnt(2)
	v_mul_f32_e32 v60, 0x42800000, v52
	v_med3_f32 v56, v56, s50, v51
	v_med3_f32 v57, v57, s50, v51
	v_mov_b32_e32 v52, v3
	v_cvt_pk_fp8_f32 v52, v56, v57
	v_mul_f32_e32 v53, 0x42800000, v53
	v_med3_f32 v56, v60, s50, v51
	v_med3_f32 v53, v53, s50, v51
	v_cvt_pk_fp8_f32 v52, v56, v53 op_sel:[0,0,1]
	s_waitcnt lgkmcnt(1)
	v_mul_f32_e32 v53, 0x42800000, v54
	v_mul_f32_e32 v54, 0x42800000, v55
	v_med3_f32 v56, v53, s50, v51
	v_med3_f32 v54, v54, s50, v51
	v_mov_b32_e32 v53, v3
	v_cvt_pk_fp8_f32 v53, v56, v54
	s_waitcnt lgkmcnt(0)
	v_mul_f32_e32 v55, 0x42800000, v58
	v_mul_f32_e32 v54, 0x42800000, v59
	v_med3_f32 v55, v55, s50, v51
	v_med3_f32 v54, v54, s50, v51
	v_cvt_pk_fp8_f32 v53, v55, v54 op_sel:[0,0,1]
	v_add_u32_e32 v54, s8, v22
	v_mov_b32_e32 v55, v3
	v_lshlrev_b64 v[54:55], 10, v[54:55]
	v_lshl_add_u64 v[54:55], v[10:11], 0, v[54:55]
	global_store_dwordx2 v[54:55], v[52:53], off
	v_add_u32_e32 v52, 0x28a0, v14
	ds_read2_b32 v[52:53], v52 offset1:1
	v_add_u32_e32 v54, 0x28a8, v14
	v_add_u32_e32 v56, 0x28b0, v14
	v_add_u32_e32 v58, 0x28b8, v14
	ds_read2_b32 v[54:55], v54 offset1:1
	ds_read2_b32 v[56:57], v56 offset1:1
	ds_read2_b32 v[58:59], v58 offset1:1
	s_waitcnt lgkmcnt(3)
	v_mul_f32_e32 v52, 0x42800000, v52
	v_mul_f32_e32 v53, 0x42800000, v53
	v_med3_f32 v60, v52, s50, v51
	v_med3_f32 v53, v53, s50, v51
	v_mov_b32_e32 v52, v3
	v_cvt_pk_fp8_f32 v52, v60, v53
	s_waitcnt lgkmcnt(2)
	v_mul_f32_e32 v54, 0x42800000, v54
	v_mul_f32_e32 v53, 0x42800000, v55
	v_med3_f32 v54, v54, s50, v51
	v_med3_f32 v53, v53, s50, v51
	v_cvt_pk_fp8_f32 v52, v54, v53 op_sel:[0,0,1]
	s_waitcnt lgkmcnt(1)
	v_mul_f32_e32 v53, 0x42800000, v56
	v_mul_f32_e32 v54, 0x42800000, v57
	v_med3_f32 v56, v53, s50, v51
	v_med3_f32 v54, v54, s50, v51
	v_mov_b32_e32 v53, v3
	v_cvt_pk_fp8_f32 v53, v56, v54
	s_waitcnt lgkmcnt(0)
	v_mul_f32_e32 v55, 0x42800000, v58
	v_mul_f32_e32 v54, 0x42800000, v59
	v_med3_f32 v55, v55, s50, v51
	v_med3_f32 v54, v54, s50, v51
	v_cvt_pk_fp8_f32 v53, v55, v54 op_sel:[0,0,1]
	v_add_u32_e32 v54, s8, v23
	v_mov_b32_e32 v55, v3
	v_lshlrev_b64 v[54:55], 10, v[54:55]
	ds_read2_b32 v[56:57], v43 offset1:1
	v_lshl_add_u64 v[54:55], v[10:11], 0, v[54:55]
	global_store_dwordx2 v[54:55], v[52:53], off
	ds_read2_b32 v[52:53], v44 offset1:1
	ds_read2_b32 v[54:55], v45 offset1:1
	ds_read2_b32 v[58:59], v46 offset1:1
	s_waitcnt lgkmcnt(3)
	v_mul_f32_e32 v56, 0x42800000, v56
	v_mul_f32_e32 v57, 0x42800000, v57
	s_waitcnt lgkmcnt(2)
	v_mul_f32_e32 v60, 0x42800000, v52
	v_med3_f32 v56, v56, s50, v51
	v_med3_f32 v57, v57, s50, v51
	v_mov_b32_e32 v52, v3
	v_cvt_pk_fp8_f32 v52, v56, v57
	v_mul_f32_e32 v53, 0x42800000, v53
	v_med3_f32 v56, v60, s50, v51
	v_med3_f32 v53, v53, s50, v51
	v_cvt_pk_fp8_f32 v52, v56, v53 op_sel:[0,0,1]
	s_waitcnt lgkmcnt(1)
	v_mul_f32_e32 v53, 0x42800000, v54
	v_mul_f32_e32 v54, 0x42800000, v55
	v_med3_f32 v56, v53, s50, v51
	v_med3_f32 v54, v54, s50, v51
	v_mov_b32_e32 v53, v3
	v_cvt_pk_fp8_f32 v53, v56, v54
	s_waitcnt lgkmcnt(0)
	v_mul_f32_e32 v55, 0x42800000, v58
	v_mul_f32_e32 v54, 0x42800000, v59
	v_med3_f32 v55, v55, s50, v51
	v_med3_f32 v54, v54, s50, v51
	v_cvt_pk_fp8_f32 v53, v55, v54 op_sel:[0,0,1]
	v_add_u32_e32 v54, s8, v24
	v_mov_b32_e32 v55, v3
	v_lshlrev_b64 v[54:55], 10, v[54:55]
	v_lshl_add_u64 v[54:55], v[10:11], 0, v[54:55]
	global_store_dwordx2 v[54:55], v[52:53], off
	v_add_u32_e32 v52, 0x38e0, v14
	ds_read2_b32 v[52:53], v52 offset1:1
	v_add_u32_e32 v54, 0x38e8, v14
	v_add_u32_e32 v56, 0x38f0, v14
	v_add_u32_e32 v58, 0x38f8, v14
	ds_read2_b32 v[54:55], v54 offset1:1
	ds_read2_b32 v[56:57], v56 offset1:1
	ds_read2_b32 v[58:59], v58 offset1:1
	s_waitcnt lgkmcnt(3)
	v_mul_f32_e32 v52, 0x42800000, v52
	v_mul_f32_e32 v53, 0x42800000, v53
	v_med3_f32 v60, v52, s50, v51
	v_med3_f32 v53, v53, s50, v51
	v_mov_b32_e32 v52, v3
	v_cvt_pk_fp8_f32 v52, v60, v53
	s_waitcnt lgkmcnt(2)
	v_mul_f32_e32 v54, 0x42800000, v54
	v_mul_f32_e32 v53, 0x42800000, v55
	v_med3_f32 v54, v54, s50, v51
	v_med3_f32 v53, v53, s50, v51
	v_cvt_pk_fp8_f32 v52, v54, v53 op_sel:[0,0,1]
	s_waitcnt lgkmcnt(1)
	v_mul_f32_e32 v53, 0x42800000, v56
	v_mul_f32_e32 v54, 0x42800000, v57
	v_med3_f32 v56, v53, s50, v51
	v_med3_f32 v54, v54, s50, v51
	v_mov_b32_e32 v53, v3
	v_cvt_pk_fp8_f32 v53, v56, v54
	s_waitcnt lgkmcnt(0)
	v_mul_f32_e32 v55, 0x42800000, v58
	v_mul_f32_e32 v54, 0x42800000, v59
	v_med3_f32 v55, v55, s50, v51
	v_med3_f32 v54, v54, s50, v51
	v_cvt_pk_fp8_f32 v53, v55, v54 op_sel:[0,0,1]
	v_add_u32_e32 v54, s8, v25
	v_mov_b32_e32 v55, v3
	v_lshlrev_b64 v[54:55], 10, v[54:55]
	v_lshl_add_u64 v[10:11], v[10:11], 0, v[54:55]
	global_store_dwordx2 v[10:11], v[52:53], off
	s_waitcnt lgkmcnt(0)

.LBB0_50:
	s_andn2_b64 vcc, exec, s[14:15]
	s_cbranch_vccnz .LBB0_52
	s_load_dwordx2 s[14:15], s[28:29], 0xa8
	s_lshl_b64 s[44:45], s[12:13], 22
	s_mul_i32 s8, s12, 0xfffe6600
	v_mov_b32_e32 v53, v3
	s_waitcnt lgkmcnt(0)
	s_add_u32 s40, s14, s44
	s_addc_u32 s42, s15, s45
	s_add_i32 s8, s84, s8
	s_and_b32 s8, s8, 0x1fc0
	s_and_b32 s44, s85, 0x3c0
	s_addk_i32 s8, 0xea00
	s_lshl_b64 s[14:15], s[12:13], 21
	s_add_u32 s45, s18, s14
	s_addc_u32 s91, s19, s15
	s_lshl_b64 s[14:15], s[8:9], 2
	s_add_u32 s14, s40, s14
	v_or_b32_e32 v52, s44, v9
	s_addc_u32 s15, s42, s15
	v_lshl_add_u64 v[10:11], s[14:15], 0, v[2:3]
	v_lshlrev_b32_e32 v52, 12, v52
	v_lshl_add_u64 v[10:11], v[10:11], 0, v[52:53]
	v_add_co_u32_e32 v56, vcc, s30, v10
	s_lshl_b32 s14, s44, 1
	s_nop 0
	v_addc_co_u32_e32 v57, vcc, 0, v11, vcc
	v_add_co_u32_e32 v60, vcc, s31, v10
	global_load_dwordx4 v[52:55], v[10:11], off nt
	s_nop 0
	global_load_dwordx4 v[56:59], v[56:57], off nt
	v_addc_co_u32_e32 v61, vcc, 0, v11, vcc
	v_add_co_u32_e32 v64, vcc, s33, v10
	s_add_u32 s14, s45, s14
	s_nop 0
	v_addc_co_u32_e32 v65, vcc, 0, v11, vcc
	v_add_co_u32_e32 v68, vcc, s34, v10
	global_load_dwordx4 v[60:63], v[60:61], off nt
	s_nop 0
	global_load_dwordx4 v[64:67], v[64:65], off nt
	v_addc_co_u32_e32 v69, vcc, 0, v11, vcc
	v_add_co_u32_e32 v72, vcc, s35, v10
	s_addc_u32 s15, s91, 0
	s_nop 0
	v_addc_co_u32_e32 v73, vcc, 0, v11, vcc
	v_add_co_u32_e32 v76, vcc, s36, v10
	global_load_dwordx4 v[68:71], v[68:69], off nt
	s_nop 0
	global_load_dwordx4 v[72:75], v[72:73], off nt
	v_addc_co_u32_e32 v77, vcc, 0, v11, vcc
	v_add_co_u32_e32 v80, vcc, s37, v10
	s_nop 1
	v_addc_co_u32_e32 v81, vcc, 0, v11, vcc
	v_add_co_u32_e32 v84, vcc, s38, v10
	global_load_dwordx4 v[76:79], v[76:77], off nt
	s_nop 0
	global_load_dwordx4 v[80:83], v[80:81], off nt
	v_addc_co_u32_e32 v85, vcc, 0, v11, vcc
	v_add_co_u32_e32 v88, vcc, s39, v10
	s_nop 1
	v_addc_co_u32_e32 v89, vcc, 0, v11, vcc
	v_add_co_u32_e32 v92, vcc, s41, v10
	global_load_dwordx4 v[84:87], v[84:85], off nt
	s_nop 0
	global_load_dwordx4 v[88:91], v[88:89], off nt
	v_addc_co_u32_e32 v93, vcc, 0, v11, vcc
	v_add_co_u32_e32 v96, vcc, s43, v10
	s_nop 1
	v_addc_co_u32_e32 v97, vcc, 0, v11, vcc
	v_add_co_u32_e32 v100, vcc, s46, v10
	global_load_dwordx4 v[92:95], v[92:93], off nt
	s_nop 0
	global_load_dwordx4 v[96:99], v[96:97], off nt
	v_addc_co_u32_e32 v101, vcc, 0, v11, vcc
	v_add_co_u32_e32 v104, vcc, s47, v10
	s_nop 1
	v_addc_co_u32_e32 v105, vcc, 0, v11, vcc
	v_add_co_u32_e32 v108, vcc, s48, v10
	global_load_dwordx4 v[100:103], v[100:101], off nt
	s_nop 0
	global_load_dwordx4 v[104:107], v[104:105], off nt
	v_addc_co_u32_e32 v109, vcc, 0, v11, vcc
	v_add_co_u32_e32 v10, vcc, s49, v10
	s_nop 1
	v_addc_co_u32_e32 v11, vcc, 0, v11, vcc
	global_load_dwordx4 v[108:111], v[108:109], off nt
	s_nop 0
	global_load_dwordx4 v[112:115], v[10:11], off nt
	v_lshlrev_b32_e32 v10, 1, v4
	v_mov_b32_e32 v11, v3
	v_lshl_add_u64 v[10:11], s[14:15], 0, v[10:11]
	s_waitcnt vmcnt(14)
	ds_write2_b32 v12, v52, v56 offset1:4
	ds_write2_b32 v12, v53, v57 offset0:65 offset1:69
	ds_write2_b32 v12, v54, v58 offset0:130 offset1:134
	ds_write2_b32 v12, v55, v59 offset0:195 offset1:199
	s_waitcnt vmcnt(12)
	ds_write2_b32 v12, v60, v64 offset0:8 offset1:12
	ds_write2_b32 v12, v61, v65 offset0:73 offset1:77
	ds_write2_b32 v12, v62, v66 offset0:138 offset1:142
	ds_write2_b32 v12, v63, v67 offset0:203 offset1:207
	s_waitcnt vmcnt(10)
	ds_write2_b32 v12, v68, v72 offset0:16 offset1:20
	ds_write2_b32 v12, v69, v73 offset0:81 offset1:85
	ds_write2_b32 v12, v70, v74 offset0:146 offset1:150
	ds_write2_b32 v12, v71, v75 offset0:211 offset1:215
	s_waitcnt vmcnt(8)
	ds_write2_b32 v12, v76, v80 offset0:24 offset1:28
	ds_write2_b32 v12, v77, v81 offset0:89 offset1:93
	ds_write2_b32 v12, v78, v82 offset0:154 offset1:158
	ds_write2_b32 v12, v79, v83 offset0:219 offset1:223
	s_waitcnt vmcnt(6)
	ds_write2_b32 v12, v84, v88 offset0:32 offset1:36
	ds_write2_b32 v12, v85, v89 offset0:97 offset1:101
	ds_write2_b32 v12, v86, v90 offset0:162 offset1:166
	ds_write2_b32 v12, v87, v91 offset0:227 offset1:231
	s_waitcnt vmcnt(4)
	ds_write2_b32 v12, v92, v96 offset0:40 offset1:44
	ds_write2_b32 v12, v93, v97 offset0:105 offset1:109
	ds_write2_b32 v12, v94, v98 offset0:170 offset1:174
	ds_write2_b32 v12, v95, v99 offset0:235 offset1:239
	s_waitcnt vmcnt(2)
	ds_write2_b32 v12, v100, v104 offset0:48 offset1:52
	ds_write2_b32 v12, v101, v105 offset0:113 offset1:117
	ds_write2_b32 v12, v102, v106 offset0:178 offset1:182
	ds_write2_b32 v12, v103, v107 offset0:243 offset1:247
	s_waitcnt vmcnt(0)
	ds_write2_b32 v12, v108, v112 offset0:56 offset1:60
	ds_write2_b32 v12, v109, v113 offset0:121 offset1:125
	ds_write2_b32 v12, v110, v114 offset0:186 offset1:190
	ds_write2_b32 v12, v111, v115 offset0:251 offset1:255
	s_waitcnt lgkmcnt(0)
	ds_read2_b32 v[52:53], v14 offset1:1
	ds_read2_b32 v[54:55], v14 offset0:2 offset1:3
	ds_read2_b32 v[56:57], v14 offset0:4 offset1:5
	ds_read2_b32 v[58:59], v14 offset0:6 offset1:7
	s_waitcnt lgkmcnt(3)
	v_cvt_pk_bf16_f32 v52, v52, v53
	s_waitcnt lgkmcnt(2)
	v_cvt_pk_bf16_f32 v53, v54, v55
	s_waitcnt lgkmcnt(1)
	v_cvt_pk_bf16_f32 v54, v56, v57
	s_waitcnt lgkmcnt(0)
	v_cvt_pk_bf16_f32 v55, v58, v59
	ds_read2_b32 v[58:59], v26 offset1:1
	ds_read2_b32 v[60:61], v26 offset0:2 offset1:3
	ds_read2_b32 v[62:63], v26 offset0:4 offset1:5
	ds_read2_b32 v[64:65], v26 offset0:6 offset1:7
	v_or_b32_e32 v56, s8, v13
	v_mov_b32_e32 v57, v3
	v_lshlrev_b64 v[56:57], 11, v[56:57]
	v_lshl_add_u64 v[56:57], v[10:11], 0, v[56:57]
	global_store_dwordx4 v[56:57], v[52:55], off
	v_or_b32_e32 v56, s8, v15
	v_mov_b32_e32 v57, v3
	s_waitcnt lgkmcnt(3)
	v_cvt_pk_bf16_f32 v52, v58, v59
	s_waitcnt lgkmcnt(2)
	v_cvt_pk_bf16_f32 v53, v60, v61
	s_waitcnt lgkmcnt(1)
	v_cvt_pk_bf16_f32 v54, v62, v63
	s_waitcnt lgkmcnt(0)
	v_cvt_pk_bf16_f32 v55, v64, v65
	ds_read2_b32 v[58:59], v27 offset1:1
	ds_read2_b32 v[60:61], v28 offset1:1
	ds_read2_b32 v[62:63], v29 offset1:1
	ds_read2_b32 v[64:65], v30 offset1:1
	v_lshlrev_b64 v[56:57], 11, v[56:57]
	v_lshl_add_u64 v[56:57], v[10:11], 0, v[56:57]
	global_store_dwordx4 v[56:57], v[52:55], off
	v_or_b32_e32 v56, s8, v16
	v_mov_b32_e32 v57, v3
	s_waitcnt lgkmcnt(3)
	v_cvt_pk_bf16_f32 v52, v58, v59
	s_waitcnt lgkmcnt(2)
	v_cvt_pk_bf16_f32 v53, v60, v61
	s_waitcnt lgkmcnt(1)
	v_cvt_pk_bf16_f32 v54, v62, v63
	s_waitcnt lgkmcnt(0)
	v_cvt_pk_bf16_f32 v55, v64, v65
	ds_read2_b32 v[58:59], v31 offset1:1
	ds_read2_b32 v[60:61], v32 offset1:1
	ds_read2_b32 v[62:63], v33 offset1:1
	ds_read2_b32 v[64:65], v34 offset1:1
	v_lshlrev_b64 v[56:57], 11, v[56:57]
	v_lshl_add_u64 v[56:57], v[10:11], 0, v[56:57]
	global_store_dwordx4 v[56:57], v[52:55], off
	v_or_b32_e32 v56, s8, v17
	v_mov_b32_e32 v57, v3
	s_waitcnt lgkmcnt(3)
	v_cvt_pk_bf16_f32 v52, v58, v59
	s_waitcnt lgkmcnt(2)
	v_cvt_pk_bf16_f32 v53, v60, v61
	s_waitcnt lgkmcnt(1)
	v_cvt_pk_bf16_f32 v54, v62, v63
	s_waitcnt lgkmcnt(0)
	v_cvt_pk_bf16_f32 v55, v64, v65
	ds_read2_b32 v[58:59], v35 offset1:1
	ds_read2_b32 v[60:61], v36 offset1:1
	ds_read2_b32 v[62:63], v37 offset1:1
	ds_read2_b32 v[64:65], v38 offset1:1
	v_lshlrev_b64 v[56:57], 11, v[56:57]
	v_lshl_add_u64 v[56:57], v[10:11], 0, v[56:57]
	global_store_dwordx4 v[56:57], v[52:55], off
	v_or_b32_e32 v56, s8, v18
	v_mov_b32_e32 v57, v3
	s_waitcnt lgkmcnt(3)
	v_cvt_pk_bf16_f32 v52, v58, v59
	s_waitcnt lgkmcnt(2)
	v_cvt_pk_bf16_f32 v53, v60, v61
	s_waitcnt lgkmcnt(1)
	v_cvt_pk_bf16_f32 v54, v62, v63
	s_waitcnt lgkmcnt(0)
	v_cvt_pk_bf16_f32 v55, v64, v65
	ds_read2_b32 v[58:59], v39 offset1:1
	ds_read2_b32 v[60:61], v40 offset1:1
	ds_read2_b32 v[62:63], v41 offset1:1
	ds_read2_b32 v[64:65], v42 offset1:1
	v_lshlrev_b64 v[56:57], 11, v[56:57]
	v_lshl_add_u64 v[56:57], v[10:11], 0, v[56:57]
	global_store_dwordx4 v[56:57], v[52:55], off
	v_or_b32_e32 v56, s8, v19
	v_mov_b32_e32 v57, v3
	s_waitcnt lgkmcnt(3)
	v_cvt_pk_bf16_f32 v52, v58, v59
	s_waitcnt lgkmcnt(2)
	v_cvt_pk_bf16_f32 v53, v60, v61
	s_waitcnt lgkmcnt(1)
	v_cvt_pk_bf16_f32 v54, v62, v63
	s_waitcnt lgkmcnt(0)
	v_cvt_pk_bf16_f32 v55, v64, v65
	ds_read2_b32 v[58:59], v43 offset1:1
	ds_read2_b32 v[60:61], v44 offset1:1
	ds_read2_b32 v[62:63], v45 offset1:1
	ds_read2_b32 v[64:65], v46 offset1:1
	v_lshlrev_b64 v[56:57], 11, v[56:57]
	v_lshl_add_u64 v[56:57], v[10:11], 0, v[56:57]
	global_store_dwordx4 v[56:57], v[52:55], off
	v_or_b32_e32 v56, s8, v20
	v_mov_b32_e32 v57, v3
	s_waitcnt lgkmcnt(3)
	v_cvt_pk_bf16_f32 v52, v58, v59
	s_waitcnt lgkmcnt(2)
	v_cvt_pk_bf16_f32 v53, v60, v61
	s_waitcnt lgkmcnt(1)
	v_cvt_pk_bf16_f32 v54, v62, v63
	s_waitcnt lgkmcnt(0)
	v_cvt_pk_bf16_f32 v55, v64, v65
	ds_read2_b32 v[58:59], v47 offset1:1
	ds_read2_b32 v[60:61], v48 offset1:1
	ds_read2_b32 v[62:63], v49 offset1:1
	ds_read2_b32 v[64:65], v50 offset1:1
	v_lshlrev_b64 v[56:57], 11, v[56:57]
	v_lshl_add_u64 v[56:57], v[10:11], 0, v[56:57]
	global_store_dwordx4 v[56:57], v[52:55], off
	v_or_b32_e32 v56, s8, v21
	v_mov_b32_e32 v57, v3
	v_lshlrev_b64 v[56:57], 11, v[56:57]
	s_waitcnt lgkmcnt(3)
	v_cvt_pk_bf16_f32 v52, v58, v59
	s_waitcnt lgkmcnt(2)
	v_cvt_pk_bf16_f32 v53, v60, v61
	s_waitcnt lgkmcnt(1)
	v_cvt_pk_bf16_f32 v54, v62, v63
	s_waitcnt lgkmcnt(0)
	v_cvt_pk_bf16_f32 v55, v64, v65
	v_lshl_add_u64 v[10:11], v[10:11], 0, v[56:57]
	global_store_dwordx4 v[10:11], v[52:55], off
	s_waitcnt lgkmcnt(0)

.LBB0_53:
	s_andn2_b64 vcc, exec, s[14:15]
	s_cbranch_vccnz .LBB0_55
	s_load_dwordx2 s[14:15], s[28:29], 0xa0
	s_lshl_b64 s[44:45], s[12:13], 22
	s_mul_i32 s8, s12, 0xfffe6600
	v_mov_b32_e32 v53, v3
	s_waitcnt lgkmcnt(0)
	s_add_u32 s40, s14, s44
	s_addc_u32 s42, s15, s45
	s_add_i32 s8, s84, s8
	s_and_b32 s8, s8, 0x1fc0
	s_and_b32 s44, s85, 0x3c0
	s_addk_i32 s8, 0xee00
	s_lshl_b64 s[14:15], s[12:13], 21
	s_add_u32 s13, s22, s14
	s_addc_u32 s45, s23, s15
	s_lshl_b64 s[14:15], s[8:9], 2
	s_add_u32 s14, s40, s14
	v_or_b32_e32 v52, s44, v9
	s_addc_u32 s15, s42, s15
	v_lshl_add_u64 v[10:11], s[14:15], 0, v[2:3]
	v_lshlrev_b32_e32 v52, 12, v52
	v_lshl_add_u64 v[10:11], v[10:11], 0, v[52:53]
	v_add_co_u32_e32 v56, vcc, s30, v10
	s_lshl_b32 s14, s44, 1
	s_nop 0
	v_addc_co_u32_e32 v57, vcc, 0, v11, vcc
	v_add_co_u32_e32 v60, vcc, s31, v10
	global_load_dwordx4 v[52:55], v[10:11], off nt
	s_nop 0
	global_load_dwordx4 v[56:59], v[56:57], off nt
	v_addc_co_u32_e32 v61, vcc, 0, v11, vcc
	v_add_co_u32_e32 v64, vcc, s33, v10
	s_add_u32 s14, s13, s14
	s_nop 0
	v_addc_co_u32_e32 v65, vcc, 0, v11, vcc
	v_add_co_u32_e32 v68, vcc, s34, v10
	global_load_dwordx4 v[60:63], v[60:61], off nt
	s_nop 0
	global_load_dwordx4 v[64:67], v[64:65], off nt
	v_addc_co_u32_e32 v69, vcc, 0, v11, vcc
	v_add_co_u32_e32 v72, vcc, s35, v10
	s_addc_u32 s15, s45, 0
	s_nop 0
	v_addc_co_u32_e32 v73, vcc, 0, v11, vcc
	v_add_co_u32_e32 v76, vcc, s36, v10
	global_load_dwordx4 v[68:71], v[68:69], off nt
	s_nop 0
	global_load_dwordx4 v[72:75], v[72:73], off nt
	v_addc_co_u32_e32 v77, vcc, 0, v11, vcc
	v_add_co_u32_e32 v80, vcc, s37, v10
	s_nop 1
	v_addc_co_u32_e32 v81, vcc, 0, v11, vcc
	v_add_co_u32_e32 v84, vcc, s38, v10
	global_load_dwordx4 v[76:79], v[76:77], off nt
	s_nop 0
	global_load_dwordx4 v[80:83], v[80:81], off nt
	v_addc_co_u32_e32 v85, vcc, 0, v11, vcc
	v_add_co_u32_e32 v88, vcc, s39, v10
	s_nop 1
	v_addc_co_u32_e32 v89, vcc, 0, v11, vcc
	v_add_co_u32_e32 v92, vcc, s41, v10
	global_load_dwordx4 v[84:87], v[84:85], off nt
	s_nop 0
	global_load_dwordx4 v[88:91], v[88:89], off nt
	v_addc_co_u32_e32 v93, vcc, 0, v11, vcc
	v_add_co_u32_e32 v96, vcc, s43, v10
	s_nop 1
	v_addc_co_u32_e32 v97, vcc, 0, v11, vcc
	v_add_co_u32_e32 v100, vcc, s46, v10
	global_load_dwordx4 v[92:95], v[92:93], off nt
	s_nop 0
	global_load_dwordx4 v[96:99], v[96:97], off nt
	v_addc_co_u32_e32 v101, vcc, 0, v11, vcc
	v_add_co_u32_e32 v104, vcc, s47, v10
	s_nop 1
	v_addc_co_u32_e32 v105, vcc, 0, v11, vcc
	v_add_co_u32_e32 v108, vcc, s48, v10
	global_load_dwordx4 v[100:103], v[100:101], off nt
	s_nop 0
	global_load_dwordx4 v[104:107], v[104:105], off nt
	v_addc_co_u32_e32 v109, vcc, 0, v11, vcc
	v_add_co_u32_e32 v10, vcc, s49, v10
	s_nop 1
	v_addc_co_u32_e32 v11, vcc, 0, v11, vcc
	global_load_dwordx4 v[108:111], v[108:109], off nt
	s_nop 0
	global_load_dwordx4 v[112:115], v[10:11], off nt
	v_lshlrev_b32_e32 v10, 1, v4
	v_mov_b32_e32 v11, v3
	v_lshl_add_u64 v[10:11], s[14:15], 0, v[10:11]
	s_waitcnt vmcnt(14)
	ds_write2_b32 v12, v52, v56 offset1:4
	ds_write2_b32 v12, v53, v57 offset0:65 offset1:69
	ds_write2_b32 v12, v54, v58 offset0:130 offset1:134
	ds_write2_b32 v12, v55, v59 offset0:195 offset1:199
	s_waitcnt vmcnt(12)
	ds_write2_b32 v12, v60, v64 offset0:8 offset1:12
	ds_write2_b32 v12, v61, v65 offset0:73 offset1:77
	ds_write2_b32 v12, v62, v66 offset0:138 offset1:142
	ds_write2_b32 v12, v63, v67 offset0:203 offset1:207
	s_waitcnt vmcnt(10)
	ds_write2_b32 v12, v68, v72 offset0:16 offset1:20
	ds_write2_b32 v12, v69, v73 offset0:81 offset1:85
	ds_write2_b32 v12, v70, v74 offset0:146 offset1:150
	ds_write2_b32 v12, v71, v75 offset0:211 offset1:215
	s_waitcnt vmcnt(8)
	ds_write2_b32 v12, v76, v80 offset0:24 offset1:28
	ds_write2_b32 v12, v77, v81 offset0:89 offset1:93
	ds_write2_b32 v12, v78, v82 offset0:154 offset1:158
	ds_write2_b32 v12, v79, v83 offset0:219 offset1:223
	s_waitcnt vmcnt(6)
	ds_write2_b32 v12, v84, v88 offset0:32 offset1:36
	ds_write2_b32 v12, v85, v89 offset0:97 offset1:101
	ds_write2_b32 v12, v86, v90 offset0:162 offset1:166
	ds_write2_b32 v12, v87, v91 offset0:227 offset1:231
	s_waitcnt vmcnt(4)
	ds_write2_b32 v12, v92, v96 offset0:40 offset1:44
	ds_write2_b32 v12, v93, v97 offset0:105 offset1:109
	ds_write2_b32 v12, v94, v98 offset0:170 offset1:174
	ds_write2_b32 v12, v95, v99 offset0:235 offset1:239
	s_waitcnt vmcnt(2)
	ds_write2_b32 v12, v100, v104 offset0:48 offset1:52
	ds_write2_b32 v12, v101, v105 offset0:113 offset1:117
	ds_write2_b32 v12, v102, v106 offset0:178 offset1:182
	ds_write2_b32 v12, v103, v107 offset0:243 offset1:247
	s_waitcnt vmcnt(0)
	ds_write2_b32 v12, v108, v112 offset0:56 offset1:60
	ds_write2_b32 v12, v109, v113 offset0:121 offset1:125
	ds_write2_b32 v12, v110, v114 offset0:186 offset1:190
	ds_write2_b32 v12, v111, v115 offset0:251 offset1:255
	s_waitcnt lgkmcnt(0)
	ds_read2_b32 v[52:53], v14 offset1:1
	ds_read2_b32 v[54:55], v14 offset0:2 offset1:3
	ds_read2_b32 v[56:57], v14 offset0:4 offset1:5
	ds_read2_b32 v[58:59], v14 offset0:6 offset1:7
	s_waitcnt lgkmcnt(3)
	v_cvt_pk_bf16_f32 v52, v52, v53
	s_waitcnt lgkmcnt(2)
	v_cvt_pk_bf16_f32 v53, v54, v55
	s_waitcnt lgkmcnt(1)
	v_cvt_pk_bf16_f32 v54, v56, v57
	s_waitcnt lgkmcnt(0)
	v_cvt_pk_bf16_f32 v55, v58, v59
	ds_read2_b32 v[58:59], v26 offset1:1
	ds_read2_b32 v[60:61], v26 offset0:2 offset1:3
	ds_read2_b32 v[62:63], v26 offset0:4 offset1:5
	ds_read2_b32 v[64:65], v26 offset0:6 offset1:7
	v_or_b32_e32 v56, s8, v13
	v_mov_b32_e32 v57, v3
	v_lshlrev_b64 v[56:57], 11, v[56:57]
	v_lshl_add_u64 v[56:57], v[10:11], 0, v[56:57]
	global_store_dwordx4 v[56:57], v[52:55], off
	v_or_b32_e32 v56, s8, v15
	v_mov_b32_e32 v57, v3
	s_waitcnt lgkmcnt(3)
	v_cvt_pk_bf16_f32 v52, v58, v59
	s_waitcnt lgkmcnt(2)
	v_cvt_pk_bf16_f32 v53, v60, v61
	s_waitcnt lgkmcnt(1)
	v_cvt_pk_bf16_f32 v54, v62, v63
	s_waitcnt lgkmcnt(0)
	v_cvt_pk_bf16_f32 v55, v64, v65
	ds_read2_b32 v[58:59], v27 offset1:1
	ds_read2_b32 v[60:61], v28 offset1:1
	ds_read2_b32 v[62:63], v29 offset1:1
	ds_read2_b32 v[64:65], v30 offset1:1
	v_lshlrev_b64 v[56:57], 11, v[56:57]
	v_lshl_add_u64 v[56:57], v[10:11], 0, v[56:57]
	global_store_dwordx4 v[56:57], v[52:55], off
	v_or_b32_e32 v56, s8, v16
	v_mov_b32_e32 v57, v3
	s_waitcnt lgkmcnt(3)
	v_cvt_pk_bf16_f32 v52, v58, v59
	s_waitcnt lgkmcnt(2)
	v_cvt_pk_bf16_f32 v53, v60, v61
	s_waitcnt lgkmcnt(1)
	v_cvt_pk_bf16_f32 v54, v62, v63
	s_waitcnt lgkmcnt(0)
	v_cvt_pk_bf16_f32 v55, v64, v65
	ds_read2_b32 v[58:59], v31 offset1:1
	ds_read2_b32 v[60:61], v32 offset1:1
	ds_read2_b32 v[62:63], v33 offset1:1
	ds_read2_b32 v[64:65], v34 offset1:1
	v_lshlrev_b64 v[56:57], 11, v[56:57]
	v_lshl_add_u64 v[56:57], v[10:11], 0, v[56:57]
	global_store_dwordx4 v[56:57], v[52:55], off
	v_or_b32_e32 v56, s8, v17
	v_mov_b32_e32 v57, v3
	s_waitcnt lgkmcnt(3)
	v_cvt_pk_bf16_f32 v52, v58, v59
	s_waitcnt lgkmcnt(2)
	v_cvt_pk_bf16_f32 v53, v60, v61
	s_waitcnt lgkmcnt(1)
	v_cvt_pk_bf16_f32 v54, v62, v63
	s_waitcnt lgkmcnt(0)
	v_cvt_pk_bf16_f32 v55, v64, v65
	ds_read2_b32 v[58:59], v35 offset1:1
	ds_read2_b32 v[60:61], v36 offset1:1
	ds_read2_b32 v[62:63], v37 offset1:1
	ds_read2_b32 v[64:65], v38 offset1:1
	v_lshlrev_b64 v[56:57], 11, v[56:57]
	v_lshl_add_u64 v[56:57], v[10:11], 0, v[56:57]
	global_store_dwordx4 v[56:57], v[52:55], off
	v_or_b32_e32 v56, s8, v18
	v_mov_b32_e32 v57, v3
	s_waitcnt lgkmcnt(3)
	v_cvt_pk_bf16_f32 v52, v58, v59
	s_waitcnt lgkmcnt(2)
	v_cvt_pk_bf16_f32 v53, v60, v61
	s_waitcnt lgkmcnt(1)
	v_cvt_pk_bf16_f32 v54, v62, v63
	s_waitcnt lgkmcnt(0)
	v_cvt_pk_bf16_f32 v55, v64, v65
	ds_read2_b32 v[58:59], v39 offset1:1
	ds_read2_b32 v[60:61], v40 offset1:1
	ds_read2_b32 v[62:63], v41 offset1:1
	ds_read2_b32 v[64:65], v42 offset1:1
	v_lshlrev_b64 v[56:57], 11, v[56:57]
	v_lshl_add_u64 v[56:57], v[10:11], 0, v[56:57]
	global_store_dwordx4 v[56:57], v[52:55], off
	v_or_b32_e32 v56, s8, v19
	v_mov_b32_e32 v57, v3
	s_waitcnt lgkmcnt(3)
	v_cvt_pk_bf16_f32 v52, v58, v59
	s_waitcnt lgkmcnt(2)
	v_cvt_pk_bf16_f32 v53, v60, v61
	s_waitcnt lgkmcnt(1)
	v_cvt_pk_bf16_f32 v54, v62, v63
	s_waitcnt lgkmcnt(0)
	v_cvt_pk_bf16_f32 v55, v64, v65
	ds_read2_b32 v[58:59], v43 offset1:1
	ds_read2_b32 v[60:61], v44 offset1:1
	ds_read2_b32 v[62:63], v45 offset1:1
	ds_read2_b32 v[64:65], v46 offset1:1
	v_lshlrev_b64 v[56:57], 11, v[56:57]
	v_lshl_add_u64 v[56:57], v[10:11], 0, v[56:57]
	global_store_dwordx4 v[56:57], v[52:55], off
	v_or_b32_e32 v56, s8, v20
	v_mov_b32_e32 v57, v3
	s_waitcnt lgkmcnt(3)
	v_cvt_pk_bf16_f32 v52, v58, v59
	s_waitcnt lgkmcnt(2)
	v_cvt_pk_bf16_f32 v53, v60, v61
	s_waitcnt lgkmcnt(1)
	v_cvt_pk_bf16_f32 v54, v62, v63
	s_waitcnt lgkmcnt(0)
	v_cvt_pk_bf16_f32 v55, v64, v65
	ds_read2_b32 v[58:59], v47 offset1:1
	ds_read2_b32 v[60:61], v48 offset1:1
	ds_read2_b32 v[62:63], v49 offset1:1
	ds_read2_b32 v[64:65], v50 offset1:1
	v_lshlrev_b64 v[56:57], 11, v[56:57]
	v_lshl_add_u64 v[56:57], v[10:11], 0, v[56:57]
	global_store_dwordx4 v[56:57], v[52:55], off
	v_or_b32_e32 v56, s8, v21
	v_mov_b32_e32 v57, v3
	v_lshlrev_b64 v[56:57], 11, v[56:57]
	s_waitcnt lgkmcnt(3)
	v_cvt_pk_bf16_f32 v52, v58, v59
	s_waitcnt lgkmcnt(2)
	v_cvt_pk_bf16_f32 v53, v60, v61
	s_waitcnt lgkmcnt(1)
	v_cvt_pk_bf16_f32 v54, v62, v63
	s_waitcnt lgkmcnt(0)
	v_cvt_pk_bf16_f32 v55, v64, v65
	v_lshl_add_u64 v[10:11], v[10:11], 0, v[56:57]
	global_store_dwordx4 v[10:11], v[52:55], off
	s_waitcnt lgkmcnt(0)

.LBB0_56:
	s_andn2_b64 vcc, exec, s[14:15]
	s_cbranch_vccnz .LBB0_58
	s_mul_i32 s13, s12, 0x280000
	s_mul_hi_i32 s8, s12, 0x280000
	s_add_u32 s13, s0, s13
	s_addc_u32 s40, s1, s8
	s_mul_i32 s8, s12, 0xfffe6600
	s_add_i32 s8, s84, s8
	s_and_b32 s14, s8, 0x1fc0
	s_and_b32 s42, s85, 0x3c0
	s_add_i32 s8, s14, 0xfffff100
	s_lshl_b32 s14, s14, 2
	v_or_b32_e32 v52, s42, v9
	s_add_u32 s14, s88, s14
	s_addc_u32 s15, s89, 0
	v_mul_u32_u24_e32 v52, 0x1300, v52
	v_lshl_add_u64 v[10:11], s[14:15], 0, v[2:3]
	v_lshlrev_b32_e32 v52, 2, v52
	v_mov_b32_e32 v53, v3
	v_lshl_add_u64 v[10:11], v[10:11], 0, v[52:53]
	s_movk_i32 s14, 0xd000
	v_add_co_u32_e32 v52, vcc, s14, v10
	s_mov_b32 s14, 0x23000
	s_nop 0
	v_addc_co_u32_e32 v53, vcc, -1, v11, vcc
	v_add_co_u32_e32 v56, vcc, s34, v10
	s_nop 1
	v_addc_co_u32_e32 v57, vcc, 0, v11, vcc
	v_add_co_u32_e32 v60, vcc, s14, v10
	s_mov_b32 s14, 0x36000
	s_nop 0
	v_addc_co_u32_e32 v61, vcc, 0, v11, vcc
	v_add_co_u32_e32 v64, vcc, s14, v10
	s_mov_b32 s14, 0x49000
	s_nop 0
	v_addc_co_u32_e32 v65, vcc, 0, v11, vcc
	v_add_co_u32_e32 v68, vcc, s14, v10
	s_mov_b32 s14, 0x5c000
	s_nop 0
	v_addc_co_u32_e32 v69, vcc, 0, v11, vcc
	v_add_co_u32_e32 v72, vcc, s14, v10
	s_mov_b32 s14, 0x6f000
	s_nop 0
	v_addc_co_u32_e32 v73, vcc, 0, v11, vcc
	v_add_co_u32_e32 v76, vcc, s14, v10
	s_mov_b32 s14, 0x82000
	s_nop 0
	v_addc_co_u32_e32 v77, vcc, 0, v11, vcc
	v_add_co_u32_e32 v80, vcc, s14, v10
	s_mov_b32 s14, 0x95000
	s_nop 0
	v_addc_co_u32_e32 v81, vcc, 0, v11, vcc
	v_add_co_u32_e32 v84, vcc, s14, v10
	s_mov_b32 s14, 0xa8000
	s_nop 0
	v_addc_co_u32_e32 v85, vcc, 0, v11, vcc
	v_add_co_u32_e32 v88, vcc, s14, v10
	s_mov_b32 s14, 0xbb000
	s_nop 0
	v_addc_co_u32_e32 v89, vcc, 0, v11, vcc
	v_add_co_u32_e32 v92, vcc, s14, v10
	s_mov_b32 s14, 0xce000
	s_nop 0
	v_addc_co_u32_e32 v93, vcc, 0, v11, vcc
	v_add_co_u32_e32 v96, vcc, s14, v10
	s_mov_b32 s14, 0xe1000
	s_nop 0
	v_addc_co_u32_e32 v97, vcc, 0, v11, vcc
	v_add_co_u32_e32 v100, vcc, s14, v10
	s_mov_b32 s14, 0xf4000
	s_nop 0
	v_addc_co_u32_e32 v101, vcc, 0, v11, vcc
	v_add_co_u32_e32 v104, vcc, s14, v10
	global_load_dwordx4 v[52:55], v[52:53], off nt
	s_nop 0
	global_load_dwordx4 v[56:59], v[56:57], off nt
	v_addc_co_u32_e32 v105, vcc, 0, v11, vcc
	v_add_co_u32_e32 v108, vcc, s52, v10
	global_load_dwordx4 v[60:63], v[60:61], off nt
	s_nop 0
	global_load_dwordx4 v[64:67], v[64:65], off nt
	v_addc_co_u32_e32 v109, vcc, 0, v11, vcc
	v_add_co_u32_e32 v10, vcc, s53, v10
	global_load_dwordx4 v[68:71], v[68:69], off nt
	s_nop 0
	global_load_dwordx4 v[72:75], v[72:73], off nt
	s_nop 0
	global_load_dwordx4 v[76:79], v[76:77], off nt
	s_nop 0
	global_load_dwordx4 v[80:83], v[80:81], off nt
	s_nop 0
	global_load_dwordx4 v[84:87], v[84:85], off nt
	s_nop 0
	global_load_dwordx4 v[88:91], v[88:89], off nt
	s_nop 0
	global_load_dwordx4 v[92:95], v[92:93], off nt
	s_nop 0
	global_load_dwordx4 v[96:99], v[96:97], off nt
	s_nop 0
	global_load_dwordx4 v[100:103], v[100:101], off nt
	s_nop 0
	global_load_dwordx4 v[104:107], v[104:105], off nt
	v_addc_co_u32_e32 v11, vcc, 0, v11, vcc
	global_load_dwordx4 v[108:111], v[108:109], off nt
	s_nop 0
	global_load_dwordx4 v[112:115], v[10:11], off nt
	s_lshl_b32 s14, s42, 1
	s_add_u32 s14, s13, s14
	s_addc_u32 s15, s40, 0
	v_lshlrev_b32_e32 v10, 1, v4
	v_mov_b32_e32 v11, v3
	v_lshl_add_u64 v[10:11], s[14:15], 0, v[10:11]
	s_waitcnt vmcnt(14)
	ds_write2_b32 v12, v52, v56 offset1:4
	ds_write2_b32 v12, v53, v57 offset0:65 offset1:69
	ds_write2_b32 v12, v54, v58 offset0:130 offset1:134
	ds_write2_b32 v12, v55, v59 offset0:195 offset1:199
	s_waitcnt vmcnt(12)
	ds_write2_b32 v12, v60, v64 offset0:8 offset1:12
	ds_write2_b32 v12, v61, v65 offset0:73 offset1:77
	ds_write2_b32 v12, v62, v66 offset0:138 offset1:142
	ds_write2_b32 v12, v63, v67 offset0:203 offset1:207
	s_waitcnt vmcnt(10)
	ds_write2_b32 v12, v68, v72 offset0:16 offset1:20
	ds_write2_b32 v12, v69, v73 offset0:81 offset1:85
	ds_write2_b32 v12, v70, v74 offset0:146 offset1:150
	ds_write2_b32 v12, v71, v75 offset0:211 offset1:215
	s_waitcnt vmcnt(8)
	ds_write2_b32 v12, v76, v80 offset0:24 offset1:28
	ds_write2_b32 v12, v77, v81 offset0:89 offset1:93
	ds_write2_b32 v12, v78, v82 offset0:154 offset1:158
	ds_write2_b32 v12, v79, v83 offset0:219 offset1:223
	s_waitcnt vmcnt(6)
	ds_write2_b32 v12, v84, v88 offset0:32 offset1:36
	ds_write2_b32 v12, v85, v89 offset0:97 offset1:101
	ds_write2_b32 v12, v86, v90 offset0:162 offset1:166
	ds_write2_b32 v12, v87, v91 offset0:227 offset1:231
	s_waitcnt vmcnt(4)
	ds_write2_b32 v12, v92, v96 offset0:40 offset1:44
	ds_write2_b32 v12, v93, v97 offset0:105 offset1:109
	ds_write2_b32 v12, v94, v98 offset0:170 offset1:174
	ds_write2_b32 v12, v95, v99 offset0:235 offset1:239
	s_waitcnt vmcnt(2)
	ds_write2_b32 v12, v100, v104 offset0:48 offset1:52
	ds_write2_b32 v12, v101, v105 offset0:113 offset1:117
	ds_write2_b32 v12, v102, v106 offset0:178 offset1:182
	ds_write2_b32 v12, v103, v107 offset0:243 offset1:247
	s_waitcnt vmcnt(0)
	ds_write2_b32 v12, v108, v112 offset0:56 offset1:60
	ds_write2_b32 v12, v109, v113 offset0:121 offset1:125
	ds_write2_b32 v12, v110, v114 offset0:186 offset1:190
	ds_write2_b32 v12, v111, v115 offset0:251 offset1:255
	s_waitcnt lgkmcnt(0)
	ds_read2_b32 v[52:53], v14 offset1:1
	ds_read2_b32 v[54:55], v14 offset0:2 offset1:3
	ds_read2_b32 v[56:57], v14 offset0:4 offset1:5
	ds_read2_b32 v[58:59], v14 offset0:6 offset1:7
	s_waitcnt lgkmcnt(3)
	v_cvt_pk_bf16_f32 v52, v52, v53
	s_waitcnt lgkmcnt(2)
	v_cvt_pk_bf16_f32 v53, v54, v55
	s_waitcnt lgkmcnt(1)
	v_cvt_pk_bf16_f32 v54, v56, v57
	s_waitcnt lgkmcnt(0)
	v_cvt_pk_bf16_f32 v55, v58, v59
	ds_read2_b32 v[58:59], v26 offset1:1
	ds_read2_b32 v[60:61], v26 offset0:2 offset1:3
	ds_read2_b32 v[62:63], v26 offset0:4 offset1:5
	ds_read2_b32 v[64:65], v26 offset0:6 offset1:7
	v_or_b32_e32 v56, s8, v13
	v_mov_b32_e32 v57, v3
	v_lshlrev_b64 v[56:57], 11, v[56:57]
	v_lshl_add_u64 v[56:57], v[10:11], 0, v[56:57]
	global_store_dwordx4 v[56:57], v[52:55], off
	v_or_b32_e32 v56, s8, v15
	v_mov_b32_e32 v57, v3
	s_waitcnt lgkmcnt(3)
	v_cvt_pk_bf16_f32 v52, v58, v59
	s_waitcnt lgkmcnt(2)
	v_cvt_pk_bf16_f32 v53, v60, v61
	s_waitcnt lgkmcnt(1)
	v_cvt_pk_bf16_f32 v54, v62, v63
	s_waitcnt lgkmcnt(0)
	v_cvt_pk_bf16_f32 v55, v64, v65
	ds_read2_b32 v[58:59], v27 offset1:1
	ds_read2_b32 v[60:61], v28 offset1:1
	ds_read2_b32 v[62:63], v29 offset1:1
	ds_read2_b32 v[64:65], v30 offset1:1
	v_lshlrev_b64 v[56:57], 11, v[56:57]
	v_lshl_add_u64 v[56:57], v[10:11], 0, v[56:57]
	global_store_dwordx4 v[56:57], v[52:55], off
	v_or_b32_e32 v56, s8, v16
	v_mov_b32_e32 v57, v3
	s_waitcnt lgkmcnt(3)
	v_cvt_pk_bf16_f32 v52, v58, v59
	s_waitcnt lgkmcnt(2)
	v_cvt_pk_bf16_f32 v53, v60, v61
	s_waitcnt lgkmcnt(1)
	v_cvt_pk_bf16_f32 v54, v62, v63
	s_waitcnt lgkmcnt(0)
	v_cvt_pk_bf16_f32 v55, v64, v65
	ds_read2_b32 v[58:59], v31 offset1:1
	ds_read2_b32 v[60:61], v32 offset1:1
	ds_read2_b32 v[62:63], v33 offset1:1
	ds_read2_b32 v[64:65], v34 offset1:1
	v_lshlrev_b64 v[56:57], 11, v[56:57]
	v_lshl_add_u64 v[56:57], v[10:11], 0, v[56:57]
	global_store_dwordx4 v[56:57], v[52:55], off
	v_or_b32_e32 v56, s8, v17
	v_mov_b32_e32 v57, v3
	s_waitcnt lgkmcnt(3)
	v_cvt_pk_bf16_f32 v52, v58, v59
	s_waitcnt lgkmcnt(2)
	v_cvt_pk_bf16_f32 v53, v60, v61
	s_waitcnt lgkmcnt(1)
	v_cvt_pk_bf16_f32 v54, v62, v63
	s_waitcnt lgkmcnt(0)
	v_cvt_pk_bf16_f32 v55, v64, v65
	ds_read2_b32 v[58:59], v35 offset1:1
	ds_read2_b32 v[60:61], v36 offset1:1
	ds_read2_b32 v[62:63], v37 offset1:1
	ds_read2_b32 v[64:65], v38 offset1:1
	v_lshlrev_b64 v[56:57], 11, v[56:57]
	v_lshl_add_u64 v[56:57], v[10:11], 0, v[56:57]
	global_store_dwordx4 v[56:57], v[52:55], off
	v_or_b32_e32 v56, s8, v18
	v_mov_b32_e32 v57, v3
	s_waitcnt lgkmcnt(3)
	v_cvt_pk_bf16_f32 v52, v58, v59
	s_waitcnt lgkmcnt(2)
	v_cvt_pk_bf16_f32 v53, v60, v61
	s_waitcnt lgkmcnt(1)
	v_cvt_pk_bf16_f32 v54, v62, v63
	s_waitcnt lgkmcnt(0)
	v_cvt_pk_bf16_f32 v55, v64, v65
	ds_read2_b32 v[58:59], v39 offset1:1
	ds_read2_b32 v[60:61], v40 offset1:1
	ds_read2_b32 v[62:63], v41 offset1:1
	ds_read2_b32 v[64:65], v42 offset1:1
	v_lshlrev_b64 v[56:57], 11, v[56:57]
	v_lshl_add_u64 v[56:57], v[10:11], 0, v[56:57]
	global_store_dwordx4 v[56:57], v[52:55], off
	v_or_b32_e32 v56, s8, v19
	v_mov_b32_e32 v57, v3
	s_waitcnt lgkmcnt(3)
	v_cvt_pk_bf16_f32 v52, v58, v59
	s_waitcnt lgkmcnt(2)
	v_cvt_pk_bf16_f32 v53, v60, v61
	s_waitcnt lgkmcnt(1)
	v_cvt_pk_bf16_f32 v54, v62, v63
	s_waitcnt lgkmcnt(0)
	v_cvt_pk_bf16_f32 v55, v64, v65
	ds_read2_b32 v[58:59], v43 offset1:1
	ds_read2_b32 v[60:61], v44 offset1:1
	ds_read2_b32 v[62:63], v45 offset1:1
	ds_read2_b32 v[64:65], v46 offset1:1
	v_lshlrev_b64 v[56:57], 11, v[56:57]
	v_lshl_add_u64 v[56:57], v[10:11], 0, v[56:57]
	global_store_dwordx4 v[56:57], v[52:55], off
	v_or_b32_e32 v56, s8, v20
	v_mov_b32_e32 v57, v3
	s_waitcnt lgkmcnt(3)
	v_cvt_pk_bf16_f32 v52, v58, v59
	s_waitcnt lgkmcnt(2)
	v_cvt_pk_bf16_f32 v53, v60, v61
	s_waitcnt lgkmcnt(1)
	v_cvt_pk_bf16_f32 v54, v62, v63
	s_waitcnt lgkmcnt(0)
	v_cvt_pk_bf16_f32 v55, v64, v65
	ds_read2_b32 v[58:59], v47 offset1:1
	ds_read2_b32 v[60:61], v48 offset1:1
	ds_read2_b32 v[62:63], v49 offset1:1
	ds_read2_b32 v[64:65], v50 offset1:1
	v_lshlrev_b64 v[56:57], 11, v[56:57]
	v_lshl_add_u64 v[56:57], v[10:11], 0, v[56:57]
	global_store_dwordx4 v[56:57], v[52:55], off
	v_or_b32_e32 v56, s8, v21
	v_mov_b32_e32 v57, v3
	v_lshlrev_b64 v[56:57], 11, v[56:57]
	s_waitcnt lgkmcnt(3)
	v_cvt_pk_bf16_f32 v52, v58, v59
	s_waitcnt lgkmcnt(2)
	v_cvt_pk_bf16_f32 v53, v60, v61
	s_waitcnt lgkmcnt(1)
	v_cvt_pk_bf16_f32 v54, v62, v63
	s_waitcnt lgkmcnt(0)
	v_cvt_pk_bf16_f32 v55, v64, v65
	v_lshl_add_u64 v[10:11], v[10:11], 0, v[56:57]
	global_store_dwordx4 v[10:11], v[52:55], off
	s_waitcnt lgkmcnt(0)

.LBB0_59:
	s_andn2_b64 vcc, exec, s[14:15]
	s_cbranch_vccnz .LBB0_61
	s_mul_i32 s8, s12, 0xfffe6600
	s_add_i32 s8, s84, s8
	s_and_b32 s14, s8, 0xfc0
	s_and_b32 s13, s85, 0x3c0
	s_add_i32 s8, s14, 0xfffffd00
	s_mul_i32 s40, s12, 0x300000
	s_mul_hi_i32 s15, s12, 0x300000
	s_add_u32 s40, s24, s40
	s_addc_u32 s42, s25, s15
	s_lshl_b32 s14, s14, 2
	v_or_b32_e32 v52, s13, v9
	s_add_u32 s14, s88, s14
	s_addc_u32 s15, s89, 0
	v_mul_u32_u24_e32 v52, 0x1300, v52
	v_lshl_add_u64 v[10:11], s[14:15], 0, v[2:3]
	v_lshlrev_b32_e32 v52, 2, v52
	v_mov_b32_e32 v53, v3
	v_lshl_add_u64 v[10:11], v[10:11], 0, v[52:53]
	v_add_co_u32_e32 v52, vcc, s54, v10
	s_add_u32 s14, s40, s13
	s_nop 0
	v_addc_co_u32_e32 v53, vcc, 0, v11, vcc
	v_add_co_u32_e32 v56, vcc, s35, v10
	s_addc_u32 s15, s42, 0
	s_nop 0
	v_addc_co_u32_e32 v57, vcc, 0, v11, vcc
	v_add_co_u32_e32 v60, vcc, s55, v10
	global_load_dwordx4 v[52:55], v[52:53], off nt
	s_nop 0
	global_load_dwordx4 v[56:59], v[56:57], off nt
	v_addc_co_u32_e32 v61, vcc, 0, v11, vcc
	v_add_co_u32_e32 v64, vcc, s56, v10
	s_nop 1
	v_addc_co_u32_e32 v65, vcc, 0, v11, vcc
	v_add_co_u32_e32 v68, vcc, s57, v10
	global_load_dwordx4 v[60:63], v[60:61], off nt
	s_nop 0
	global_load_dwordx4 v[64:67], v[64:65], off nt
	v_addc_co_u32_e32 v69, vcc, 0, v11, vcc
	v_add_co_u32_e32 v72, vcc, s51, v10
	s_nop 1
	v_addc_co_u32_e32 v73, vcc, 0, v11, vcc
	v_add_co_u32_e32 v76, vcc, s58, v10
	global_load_dwordx4 v[68:71], v[68:69], off nt
	s_nop 0
	global_load_dwordx4 v[72:75], v[72:73], off nt
	v_addc_co_u32_e32 v77, vcc, 0, v11, vcc
	v_add_co_u32_e32 v80, vcc, s59, v10
	s_nop 1
	v_addc_co_u32_e32 v81, vcc, 0, v11, vcc
	v_add_co_u32_e32 v84, vcc, s60, v10
	s_nop 1
	v_addc_co_u32_e32 v85, vcc, 0, v11, vcc
	v_add_co_u32_e32 v88, vcc, s61, v10
	s_nop 1
	v_addc_co_u32_e32 v89, vcc, 0, v11, vcc
	v_add_co_u32_e32 v92, vcc, s62, v10
	s_nop 1
	v_addc_co_u32_e32 v93, vcc, 0, v11, vcc
	v_add_co_u32_e32 v96, vcc, s63, v10
	s_nop 1
	v_addc_co_u32_e32 v97, vcc, 0, v11, vcc
	v_add_co_u32_e32 v100, vcc, s64, v10
	s_nop 1
	v_addc_co_u32_e32 v101, vcc, 0, v11, vcc
	v_add_co_u32_e32 v104, vcc, s65, v10
	s_nop 1
	v_addc_co_u32_e32 v105, vcc, 0, v11, vcc
	v_add_co_u32_e32 v108, vcc, s66, v10
	global_load_dwordx4 v[76:79], v[76:77], off nt
	s_nop 0
	global_load_dwordx4 v[80:83], v[80:81], off nt
	s_nop 0
	global_load_dwordx4 v[84:87], v[84:85], off nt
	s_nop 0
	global_load_dwordx4 v[88:91], v[88:89], off nt
	s_nop 0
	global_load_dwordx4 v[92:95], v[92:93], off nt
	s_nop 0
	global_load_dwordx4 v[96:99], v[96:97], off nt
	s_nop 0
	global_load_dwordx4 v[100:103], v[100:101], off nt
	s_nop 0
	global_load_dwordx4 v[104:107], v[104:105], off nt
	v_addc_co_u32_e32 v109, vcc, 0, v11, vcc
	v_add_co_u32_e32 v10, vcc, s67, v10
	s_nop 1
	v_addc_co_u32_e32 v11, vcc, 0, v11, vcc
	global_load_dwordx4 v[108:111], v[108:109], off nt
	s_nop 0
	global_load_dwordx4 v[112:115], v[10:11], off nt
	v_lshl_add_u64 v[10:11], s[14:15], 0, v[4:5]
	s_waitcnt vmcnt(14)
	ds_write2_b32 v12, v52, v56 offset1:4
	ds_write2_b32 v12, v53, v57 offset0:65 offset1:69
	ds_write2_b32 v12, v54, v58 offset0:130 offset1:134
	ds_write2_b32 v12, v55, v59 offset0:195 offset1:199
	s_waitcnt vmcnt(12)
	ds_write2_b32 v12, v60, v64 offset0:8 offset1:12
	ds_write2_b32 v12, v61, v65 offset0:73 offset1:77
	ds_write2_b32 v12, v62, v66 offset0:138 offset1:142
	ds_write2_b32 v12, v63, v67 offset0:203 offset1:207
	s_waitcnt vmcnt(10)
	ds_write2_b32 v12, v68, v72 offset0:16 offset1:20
	ds_write2_b32 v12, v69, v73 offset0:81 offset1:85
	ds_write2_b32 v12, v70, v74 offset0:146 offset1:150
	ds_write2_b32 v12, v71, v75 offset0:211 offset1:215
	s_waitcnt vmcnt(8)
	ds_write2_b32 v12, v76, v80 offset0:24 offset1:28
	ds_write2_b32 v12, v77, v81 offset0:89 offset1:93
	ds_write2_b32 v12, v78, v82 offset0:154 offset1:158
	ds_write2_b32 v12, v79, v83 offset0:219 offset1:223
	s_waitcnt vmcnt(6)
	ds_write2_b32 v12, v84, v88 offset0:32 offset1:36
	ds_write2_b32 v12, v85, v89 offset0:97 offset1:101
	ds_write2_b32 v12, v86, v90 offset0:162 offset1:166
	ds_write2_b32 v12, v87, v91 offset0:227 offset1:231
	s_waitcnt vmcnt(4)
	ds_write2_b32 v12, v92, v96 offset0:40 offset1:44
	ds_write2_b32 v12, v93, v97 offset0:105 offset1:109
	ds_write2_b32 v12, v94, v98 offset0:170 offset1:174
	ds_write2_b32 v12, v95, v99 offset0:235 offset1:239
	s_waitcnt vmcnt(2)
	ds_write2_b32 v12, v100, v104 offset0:48 offset1:52
	ds_write2_b32 v12, v101, v105 offset0:113 offset1:117
	ds_write2_b32 v12, v102, v106 offset0:178 offset1:182
	ds_write2_b32 v12, v103, v107 offset0:243 offset1:247
	s_waitcnt vmcnt(0)
	ds_write2_b32 v12, v108, v112 offset0:56 offset1:60
	ds_write2_b32 v12, v109, v113 offset0:121 offset1:125
	ds_write2_b32 v12, v110, v114 offset0:186 offset1:190
	ds_write2_b32 v12, v111, v115 offset0:251 offset1:255
	s_waitcnt lgkmcnt(0)
	ds_read2_b32 v[52:53], v14 offset1:1
	ds_read2_b32 v[54:55], v14 offset0:2 offset1:3
	ds_read2_b32 v[56:57], v14 offset0:4 offset1:5
	ds_read2_b32 v[58:59], v14 offset0:6 offset1:7
	s_waitcnt lgkmcnt(2)
	v_mul_f32_e32 v54, 0x42800000, v54
	v_mul_f32_e32 v52, 0x42800000, v52
	v_mul_f32_e32 v53, 0x42800000, v53
	v_med3_f32 v60, v52, s50, v51
	v_med3_f32 v53, v53, s50, v51
	v_mov_b32_e32 v52, v3
	v_cvt_pk_fp8_f32 v52, v60, v53
	v_mul_f32_e32 v53, 0x42800000, v55
	v_med3_f32 v54, v54, s50, v51
	v_med3_f32 v53, v53, s50, v51
	v_cvt_pk_fp8_f32 v52, v54, v53 op_sel:[0,0,1]
	s_waitcnt lgkmcnt(1)
	v_mul_f32_e32 v53, 0x42800000, v56
	v_mul_f32_e32 v54, 0x42800000, v57
	v_med3_f32 v56, v53, s50, v51
	v_med3_f32 v54, v54, s50, v51
	v_mov_b32_e32 v53, v3
	v_cvt_pk_fp8_f32 v53, v56, v54
	s_waitcnt lgkmcnt(0)
	v_mul_f32_e32 v55, 0x42800000, v58
	v_mul_f32_e32 v54, 0x42800000, v59
	v_med3_f32 v55, v55, s50, v51
	v_med3_f32 v54, v54, s50, v51
	v_cvt_pk_fp8_f32 v53, v55, v54 op_sel:[0,0,1]
	v_or_b32_e32 v54, s8, v13
	v_mov_b32_e32 v55, v3
	v_lshlrev_b64 v[54:55], 10, v[54:55]
	ds_read2_b32 v[56:57], v26 offset1:1
	v_lshl_add_u64 v[54:55], v[10:11], 0, v[54:55]
	global_store_dwordx2 v[54:55], v[52:53], off
	ds_read2_b32 v[52:53], v26 offset0:2 offset1:3
	ds_read2_b32 v[54:55], v26 offset0:4 offset1:5
	ds_read2_b32 v[58:59], v26 offset0:6 offset1:7
	s_waitcnt lgkmcnt(3)
	v_mul_f32_e32 v56, 0x42800000, v56
	v_mul_f32_e32 v57, 0x42800000, v57
	s_waitcnt lgkmcnt(2)
	v_mul_f32_e32 v60, 0x42800000, v52
	v_med3_f32 v56, v56, s50, v51
	v_med3_f32 v57, v57, s50, v51
	v_mov_b32_e32 v52, v3
	v_cvt_pk_fp8_f32 v52, v56, v57
	v_mul_f32_e32 v53, 0x42800000, v53
	v_med3_f32 v56, v60, s50, v51
	v_med3_f32 v53, v53, s50, v51
	v_cvt_pk_fp8_f32 v52, v56, v53 op_sel:[0,0,1]
	s_waitcnt lgkmcnt(1)
	v_mul_f32_e32 v53, 0x42800000, v54
	v_mul_f32_e32 v54, 0x42800000, v55
	v_med3_f32 v56, v53, s50, v51
	v_med3_f32 v54, v54, s50, v51
	v_mov_b32_e32 v53, v3
	v_cvt_pk_fp8_f32 v53, v56, v54
	s_waitcnt lgkmcnt(0)
	v_mul_f32_e32 v55, 0x42800000, v58
	v_mul_f32_e32 v54, 0x42800000, v59
	v_med3_f32 v55, v55, s50, v51
	v_med3_f32 v54, v54, s50, v51
	v_cvt_pk_fp8_f32 v53, v55, v54 op_sel:[0,0,1]
	v_or_b32_e32 v54, s8, v15
	v_mov_b32_e32 v55, v3
	v_lshlrev_b64 v[54:55], 10, v[54:55]
	ds_read2_b32 v[56:57], v27 offset1:1
	v_lshl_add_u64 v[54:55], v[10:11], 0, v[54:55]
	global_store_dwordx2 v[54:55], v[52:53], off
	ds_read2_b32 v[52:53], v28 offset1:1
	ds_read2_b32 v[54:55], v29 offset1:1
	ds_read2_b32 v[58:59], v30 offset1:1
	s_waitcnt lgkmcnt(3)
	v_mul_f32_e32 v56, 0x42800000, v56
	v_mul_f32_e32 v57, 0x42800000, v57
	s_waitcnt lgkmcnt(2)
	v_mul_f32_e32 v60, 0x42800000, v52
	v_med3_f32 v56, v56, s50, v51
	v_med3_f32 v57, v57, s50, v51
	v_mov_b32_e32 v52, v3
	v_cvt_pk_fp8_f32 v52, v56, v57
	v_mul_f32_e32 v53, 0x42800000, v53
	v_med3_f32 v56, v60, s50, v51
	v_med3_f32 v53, v53, s50, v51
	v_cvt_pk_fp8_f32 v52, v56, v53 op_sel:[0,0,1]
	s_waitcnt lgkmcnt(1)
	v_mul_f32_e32 v53, 0x42800000, v54
	v_mul_f32_e32 v54, 0x42800000, v55
	v_med3_f32 v56, v53, s50, v51
	v_med3_f32 v54, v54, s50, v51
	v_mov_b32_e32 v53, v3
	v_cvt_pk_fp8_f32 v53, v56, v54
	s_waitcnt lgkmcnt(0)
	v_mul_f32_e32 v55, 0x42800000, v58
	v_mul_f32_e32 v54, 0x42800000, v59
	v_med3_f32 v55, v55, s50, v51
	v_med3_f32 v54, v54, s50, v51
	v_cvt_pk_fp8_f32 v53, v55, v54 op_sel:[0,0,1]
	v_or_b32_e32 v54, s8, v16
	v_mov_b32_e32 v55, v3
	v_lshlrev_b64 v[54:55], 10, v[54:55]
	ds_read2_b32 v[56:57], v31 offset1:1
	v_lshl_add_u64 v[54:55], v[10:11], 0, v[54:55]
	global_store_dwordx2 v[54:55], v[52:53], off
	ds_read2_b32 v[52:53], v32 offset1:1
	ds_read2_b32 v[54:55], v33 offset1:1
	ds_read2_b32 v[58:59], v34 offset1:1
	s_waitcnt lgkmcnt(3)
	v_mul_f32_e32 v56, 0x42800000, v56
	v_mul_f32_e32 v57, 0x42800000, v57
	s_waitcnt lgkmcnt(2)
	v_mul_f32_e32 v60, 0x42800000, v52
	v_med3_f32 v56, v56, s50, v51
	v_med3_f32 v57, v57, s50, v51
	v_mov_b32_e32 v52, v3
	v_cvt_pk_fp8_f32 v52, v56, v57
	v_mul_f32_e32 v53, 0x42800000, v53
	v_med3_f32 v56, v60, s50, v51
	v_med3_f32 v53, v53, s50, v51
	v_cvt_pk_fp8_f32 v52, v56, v53 op_sel:[0,0,1]
	s_waitcnt lgkmcnt(1)
	v_mul_f32_e32 v53, 0x42800000, v54
	v_mul_f32_e32 v54, 0x42800000, v55
	v_med3_f32 v56, v53, s50, v51
	v_med3_f32 v54, v54, s50, v51
	v_mov_b32_e32 v53, v3
	v_cvt_pk_fp8_f32 v53, v56, v54
	s_waitcnt lgkmcnt(0)
	v_mul_f32_e32 v55, 0x42800000, v58
	v_mul_f32_e32 v54, 0x42800000, v59
	v_med3_f32 v55, v55, s50, v51
	v_med3_f32 v54, v54, s50, v51
	v_cvt_pk_fp8_f32 v53, v55, v54 op_sel:[0,0,1]
	v_or_b32_e32 v54, s8, v17
	v_mov_b32_e32 v55, v3
	v_lshlrev_b64 v[54:55], 10, v[54:55]
	ds_read2_b32 v[56:57], v35 offset1:1
	v_lshl_add_u64 v[54:55], v[10:11], 0, v[54:55]
	global_store_dwordx2 v[54:55], v[52:53], off
	ds_read2_b32 v[52:53], v36 offset1:1
	ds_read2_b32 v[54:55], v37 offset1:1
	ds_read2_b32 v[58:59], v38 offset1:1
	s_waitcnt lgkmcnt(3)
	v_mul_f32_e32 v56, 0x42800000, v56
	v_mul_f32_e32 v57, 0x42800000, v57
	s_waitcnt lgkmcnt(2)
	v_mul_f32_e32 v60, 0x42800000, v52
	v_med3_f32 v56, v56, s50, v51
	v_med3_f32 v57, v57, s50, v51
	v_mov_b32_e32 v52, v3
	v_cvt_pk_fp8_f32 v52, v56, v57
	v_mul_f32_e32 v53, 0x42800000, v53
	v_med3_f32 v56, v60, s50, v51
	v_med3_f32 v53, v53, s50, v51
	v_cvt_pk_fp8_f32 v52, v56, v53 op_sel:[0,0,1]
	s_waitcnt lgkmcnt(1)
	v_mul_f32_e32 v53, 0x42800000, v54
	v_mul_f32_e32 v54, 0x42800000, v55
	v_med3_f32 v56, v53, s50, v51
	v_med3_f32 v54, v54, s50, v51
	v_mov_b32_e32 v53, v3
	v_cvt_pk_fp8_f32 v53, v56, v54
	s_waitcnt lgkmcnt(0)
	v_mul_f32_e32 v55, 0x42800000, v58
	v_mul_f32_e32 v54, 0x42800000, v59
	v_med3_f32 v55, v55, s50, v51
	v_med3_f32 v54, v54, s50, v51
	v_cvt_pk_fp8_f32 v53, v55, v54 op_sel:[0,0,1]
	v_or_b32_e32 v54, s8, v18
	v_mov_b32_e32 v55, v3
	v_lshlrev_b64 v[54:55], 10, v[54:55]
	ds_read2_b32 v[56:57], v39 offset1:1
	v_lshl_add_u64 v[54:55], v[10:11], 0, v[54:55]
	global_store_dwordx2 v[54:55], v[52:53], off
	ds_read2_b32 v[52:53], v40 offset1:1
	ds_read2_b32 v[54:55], v41 offset1:1
	ds_read2_b32 v[58:59], v42 offset1:1
	s_waitcnt lgkmcnt(3)
	v_mul_f32_e32 v56, 0x42800000, v56
	v_mul_f32_e32 v57, 0x42800000, v57
	s_waitcnt lgkmcnt(2)
	v_mul_f32_e32 v60, 0x42800000, v52
	v_med3_f32 v56, v56, s50, v51
	v_med3_f32 v57, v57, s50, v51
	v_mov_b32_e32 v52, v3
	v_cvt_pk_fp8_f32 v52, v56, v57
	v_mul_f32_e32 v53, 0x42800000, v53
	v_med3_f32 v56, v60, s50, v51
	v_med3_f32 v53, v53, s50, v51
	v_cvt_pk_fp8_f32 v52, v56, v53 op_sel:[0,0,1]
	s_waitcnt lgkmcnt(1)
	v_mul_f32_e32 v53, 0x42800000, v54
	v_mul_f32_e32 v54, 0x42800000, v55
	v_med3_f32 v56, v53, s50, v51
	v_med3_f32 v54, v54, s50, v51
	v_mov_b32_e32 v53, v3
	v_cvt_pk_fp8_f32 v53, v56, v54
	s_waitcnt lgkmcnt(0)
	v_mul_f32_e32 v55, 0x42800000, v58
	v_mul_f32_e32 v54, 0x42800000, v59
	v_med3_f32 v55, v55, s50, v51
	v_med3_f32 v54, v54, s50, v51
	v_cvt_pk_fp8_f32 v53, v55, v54 op_sel:[0,0,1]
	v_or_b32_e32 v54, s8, v19
	v_mov_b32_e32 v55, v3
	v_lshlrev_b64 v[54:55], 10, v[54:55]
	ds_read2_b32 v[56:57], v43 offset1:1
	v_lshl_add_u64 v[54:55], v[10:11], 0, v[54:55]
	global_store_dwordx2 v[54:55], v[52:53], off
	ds_read2_b32 v[52:53], v44 offset1:1
	ds_read2_b32 v[54:55], v45 offset1:1
	ds_read2_b32 v[58:59], v46 offset1:1
	s_waitcnt lgkmcnt(3)
	v_mul_f32_e32 v56, 0x42800000, v56
	v_mul_f32_e32 v57, 0x42800000, v57
	s_waitcnt lgkmcnt(2)
	v_mul_f32_e32 v60, 0x42800000, v52
	v_med3_f32 v56, v56, s50, v51
	v_med3_f32 v57, v57, s50, v51
	v_mov_b32_e32 v52, v3
	v_cvt_pk_fp8_f32 v52, v56, v57
	v_mul_f32_e32 v53, 0x42800000, v53
	v_med3_f32 v56, v60, s50, v51
	v_med3_f32 v53, v53, s50, v51
	v_cvt_pk_fp8_f32 v52, v56, v53 op_sel:[0,0,1]
	s_waitcnt lgkmcnt(1)
	v_mul_f32_e32 v53, 0x42800000, v54
	v_mul_f32_e32 v54, 0x42800000, v55
	v_med3_f32 v56, v53, s50, v51
	v_med3_f32 v54, v54, s50, v51
	v_mov_b32_e32 v53, v3
	v_cvt_pk_fp8_f32 v53, v56, v54
	s_waitcnt lgkmcnt(0)
	v_mul_f32_e32 v55, 0x42800000, v58
	v_mul_f32_e32 v54, 0x42800000, v59
	v_med3_f32 v55, v55, s50, v51
	v_med3_f32 v54, v54, s50, v51
	v_cvt_pk_fp8_f32 v53, v55, v54 op_sel:[0,0,1]
	v_or_b32_e32 v54, s8, v20
	v_mov_b32_e32 v55, v3
	v_lshlrev_b64 v[54:55], 10, v[54:55]
	ds_read2_b32 v[56:57], v47 offset1:1
	v_lshl_add_u64 v[54:55], v[10:11], 0, v[54:55]
	global_store_dwordx2 v[54:55], v[52:53], off
	ds_read2_b32 v[52:53], v48 offset1:1
	ds_read2_b32 v[54:55], v49 offset1:1
	ds_read2_b32 v[58:59], v50 offset1:1
	s_waitcnt lgkmcnt(3)
	v_mul_f32_e32 v56, 0x42800000, v56
	v_mul_f32_e32 v57, 0x42800000, v57
	s_waitcnt lgkmcnt(2)
	v_mul_f32_e32 v60, 0x42800000, v52
	v_med3_f32 v56, v56, s50, v51
	v_med3_f32 v57, v57, s50, v51
	v_mov_b32_e32 v52, v3
	v_cvt_pk_fp8_f32 v52, v56, v57
	v_mul_f32_e32 v53, 0x42800000, v53
	v_med3_f32 v56, v60, s50, v51
	v_med3_f32 v53, v53, s50, v51
	v_cvt_pk_fp8_f32 v52, v56, v53 op_sel:[0,0,1]
	s_waitcnt lgkmcnt(1)
	v_mul_f32_e32 v53, 0x42800000, v54
	v_mul_f32_e32 v54, 0x42800000, v55
	v_med3_f32 v56, v53, s50, v51
	v_med3_f32 v54, v54, s50, v51
	v_mov_b32_e32 v53, v3
	v_cvt_pk_fp8_f32 v53, v56, v54
	s_waitcnt lgkmcnt(0)
	v_mul_f32_e32 v55, 0x42800000, v58
	v_mul_f32_e32 v54, 0x42800000, v59
	v_med3_f32 v55, v55, s50, v51
	v_med3_f32 v54, v54, s50, v51
	v_cvt_pk_fp8_f32 v53, v55, v54 op_sel:[0,0,1]
	v_or_b32_e32 v54, s8, v21
	v_mov_b32_e32 v55, v3
	v_lshlrev_b64 v[54:55], 10, v[54:55]
	v_lshl_add_u64 v[10:11], v[10:11], 0, v[54:55]
	global_store_dwordx2 v[10:11], v[52:53], off
	s_waitcnt lgkmcnt(0)

.LBB0_62:
	s_andn2_b64 vcc, exec, s[14:15]
	s_cbranch_vccnz .LBB0_39
	s_mul_hi_i32 s8, s12, 0x780000
	s_mul_i32 s12, s12, 0x780000
	s_add_u32 s40, s26, s12
	s_addc_u32 s8, s27, s8
	s_bfe_u32 s12, s90, 0x4001b
	s_add_i32 s12, s90, s12
	s_sext_i32_i16 s13, s12
	s_and_b32 s12, s12, 0xfff0
	s_sub_i32 s12, s90, s12
	s_sext_i32_i16 s12, s12
	s_lshl_b32 s42, s12, 6
	s_lshl_b32 s12, s13, 2
	s_andn2_b32 s12, s12, 63
	s_ashr_i32 s13, s12, 31
	s_lshl_b64 s[14:15], s[12:13], 2
	v_or_b32_e32 v52, s42, v9
	s_add_u32 s14, s88, s14
	s_addc_u32 s15, s89, s15
	v_mul_i32_i24_e32 v52, 0x1300, v52
	v_lshl_add_u64 v[10:11], s[14:15], 0, v[2:3]
	v_ashrrev_i32_e32 v53, 31, v52
	v_lshl_add_u64 v[10:11], v[52:53], 2, v[10:11]
	v_add_co_u32_e32 v56, vcc, s68, v10
	s_ashr_i32 s13, s42, 31
	s_nop 0
	v_addc_co_u32_e32 v57, vcc, 0, v11, vcc
	v_add_co_u32_e32 v60, vcc, s69, v10
	global_load_dwordx4 v[52:55], v[10:11], off nt
	s_nop 0
	global_load_dwordx4 v[56:59], v[56:57], off nt
	v_addc_co_u32_e32 v61, vcc, 0, v11, vcc
	v_add_co_u32_e32 v64, vcc, s70, v10
	s_add_u32 s14, s40, s42
	s_nop 0
	v_addc_co_u32_e32 v65, vcc, 0, v11, vcc
	v_add_co_u32_e32 v68, vcc, s71, v10
	global_load_dwordx4 v[60:63], v[60:61], off nt
	s_nop 0
	global_load_dwordx4 v[64:67], v[64:65], off nt
	v_addc_co_u32_e32 v69, vcc, 0, v11, vcc
	v_add_co_u32_e32 v72, vcc, s72, v10
	s_addc_u32 s15, s8, s13
	s_nop 0
	v_addc_co_u32_e32 v73, vcc, 0, v11, vcc
	v_add_co_u32_e32 v76, vcc, s73, v10
	global_load_dwordx4 v[68:71], v[68:69], off nt
	s_nop 0
	global_load_dwordx4 v[72:75], v[72:73], off nt
	v_addc_co_u32_e32 v77, vcc, 0, v11, vcc
	v_add_co_u32_e32 v80, vcc, s74, v10
	s_nop 1
	v_addc_co_u32_e32 v81, vcc, 0, v11, vcc
	v_add_co_u32_e32 v84, vcc, s75, v10
	global_load_dwordx4 v[76:79], v[76:77], off nt
	s_nop 0
	global_load_dwordx4 v[80:83], v[80:81], off nt
	v_addc_co_u32_e32 v85, vcc, 0, v11, vcc
	v_add_co_u32_e32 v88, vcc, s76, v10
	s_nop 1
	v_addc_co_u32_e32 v89, vcc, 0, v11, vcc
	v_add_co_u32_e32 v92, vcc, s77, v10
	s_nop 1
	v_addc_co_u32_e32 v93, vcc, 0, v11, vcc
	v_add_co_u32_e32 v96, vcc, s78, v10
	s_nop 1
	v_addc_co_u32_e32 v97, vcc, 0, v11, vcc
	v_add_co_u32_e32 v100, vcc, s79, v10
	global_load_dwordx4 v[84:87], v[84:85], off nt
	s_nop 0
	global_load_dwordx4 v[88:91], v[88:89], off nt
	s_nop 0
	global_load_dwordx4 v[92:95], v[92:93], off nt
	s_nop 0
	global_load_dwordx4 v[96:99], v[96:97], off nt
	v_addc_co_u32_e32 v101, vcc, 0, v11, vcc
	v_add_co_u32_e32 v104, vcc, s80, v10
	s_nop 1
	v_addc_co_u32_e32 v105, vcc, 0, v11, vcc
	v_add_co_u32_e32 v108, vcc, s81, v10
	global_load_dwordx4 v[100:103], v[100:101], off nt
	s_nop 0
	global_load_dwordx4 v[104:107], v[104:105], off nt
	v_addc_co_u32_e32 v109, vcc, 0, v11, vcc
	v_add_co_u32_e32 v10, vcc, s82, v10
	s_nop 1
	v_addc_co_u32_e32 v11, vcc, 0, v11, vcc
	global_load_dwordx4 v[108:111], v[108:109], off nt
	s_nop 0
	global_load_dwordx4 v[112:115], v[10:11], off nt
	v_lshl_add_u64 v[10:11], s[14:15], 0, v[4:5]
	s_waitcnt vmcnt(14)
	ds_write2_b32 v12, v52, v56 offset1:4
	ds_write2_b32 v12, v53, v57 offset0:65 offset1:69
	ds_write2_b32 v12, v54, v58 offset0:130 offset1:134
	ds_write2_b32 v12, v55, v59 offset0:195 offset1:199
	s_waitcnt vmcnt(12)
	ds_write2_b32 v12, v60, v64 offset0:8 offset1:12
	ds_write2_b32 v12, v61, v65 offset0:73 offset1:77
	ds_write2_b32 v12, v62, v66 offset0:138 offset1:142
	ds_write2_b32 v12, v63, v67 offset0:203 offset1:207
	s_waitcnt vmcnt(10)
	ds_write2_b32 v12, v68, v72 offset0:16 offset1:20
	ds_write2_b32 v12, v69, v73 offset0:81 offset1:85
	ds_write2_b32 v12, v70, v74 offset0:146 offset1:150
	ds_write2_b32 v12, v71, v75 offset0:211 offset1:215
	s_waitcnt vmcnt(8)
	ds_write2_b32 v12, v76, v80 offset0:24 offset1:28
	ds_write2_b32 v12, v77, v81 offset0:89 offset1:93
	ds_write2_b32 v12, v78, v82 offset0:154 offset1:158
	ds_write2_b32 v12, v79, v83 offset0:219 offset1:223
	s_waitcnt vmcnt(6)
	ds_write2_b32 v12, v84, v88 offset0:32 offset1:36
	ds_write2_b32 v12, v85, v89 offset0:97 offset1:101
	ds_write2_b32 v12, v86, v90 offset0:162 offset1:166
	ds_write2_b32 v12, v87, v91 offset0:227 offset1:231
	s_waitcnt vmcnt(4)
	ds_write2_b32 v12, v92, v96 offset0:40 offset1:44
	ds_write2_b32 v12, v93, v97 offset0:105 offset1:109
	ds_write2_b32 v12, v94, v98 offset0:170 offset1:174
	ds_write2_b32 v12, v95, v99 offset0:235 offset1:239
	s_waitcnt vmcnt(2)
	ds_write2_b32 v12, v100, v104 offset0:48 offset1:52
	ds_write2_b32 v12, v101, v105 offset0:113 offset1:117
	ds_write2_b32 v12, v102, v106 offset0:178 offset1:182
	ds_write2_b32 v12, v103, v107 offset0:243 offset1:247
	s_waitcnt vmcnt(0)
	ds_write2_b32 v12, v108, v112 offset0:56 offset1:60
	ds_write2_b32 v12, v109, v113 offset0:121 offset1:125
	ds_write2_b32 v12, v110, v114 offset0:186 offset1:190
	ds_write2_b32 v12, v111, v115 offset0:251 offset1:255
	s_waitcnt lgkmcnt(0)
	ds_read2_b32 v[52:53], v14 offset1:1
	ds_read2_b32 v[54:55], v14 offset0:2 offset1:3
	ds_read2_b32 v[56:57], v14 offset0:4 offset1:5
	ds_read2_b32 v[58:59], v14 offset0:6 offset1:7
	s_waitcnt lgkmcnt(2)
	v_mul_f32_e32 v54, 0x42800000, v54
	v_mul_f32_e32 v52, 0x42800000, v52
	v_mul_f32_e32 v53, 0x42800000, v53
	v_med3_f32 v60, v52, s50, v51
	v_med3_f32 v53, v53, s50, v51
	v_mov_b32_e32 v52, v3
	v_cvt_pk_fp8_f32 v52, v60, v53
	v_mul_f32_e32 v53, 0x42800000, v55
	v_med3_f32 v54, v54, s50, v51
	v_med3_f32 v53, v53, s50, v51
	v_cvt_pk_fp8_f32 v52, v54, v53 op_sel:[0,0,1]
	s_waitcnt lgkmcnt(1)
	v_mul_f32_e32 v53, 0x42800000, v56
	v_mul_f32_e32 v54, 0x42800000, v57
	v_med3_f32 v56, v53, s50, v51
	v_med3_f32 v54, v54, s50, v51
	v_mov_b32_e32 v53, v3
	v_cvt_pk_fp8_f32 v53, v56, v54
	s_waitcnt lgkmcnt(0)
	v_mul_f32_e32 v55, 0x42800000, v58
	v_mul_f32_e32 v54, 0x42800000, v59
	v_med3_f32 v55, v55, s50, v51
	v_med3_f32 v54, v54, s50, v51
	v_cvt_pk_fp8_f32 v53, v55, v54 op_sel:[0,0,1]
	v_or_b32_e32 v54, s12, v13
	v_ashrrev_i32_e32 v55, 31, v54
	v_lshlrev_b64 v[54:55], 10, v[54:55]
	ds_read2_b32 v[56:57], v26 offset1:1
	v_lshl_add_u64 v[54:55], v[10:11], 0, v[54:55]
	global_store_dwordx2 v[54:55], v[52:53], off
	ds_read2_b32 v[52:53], v26 offset0:2 offset1:3
	ds_read2_b32 v[54:55], v26 offset0:4 offset1:5
	ds_read2_b32 v[58:59], v26 offset0:6 offset1:7
	s_waitcnt lgkmcnt(3)
	v_mul_f32_e32 v56, 0x42800000, v56
	v_mul_f32_e32 v57, 0x42800000, v57
	s_waitcnt lgkmcnt(2)
	v_mul_f32_e32 v60, 0x42800000, v52
	v_med3_f32 v56, v56, s50, v51
	v_med3_f32 v57, v57, s50, v51
	v_mov_b32_e32 v52, v3
	v_cvt_pk_fp8_f32 v52, v56, v57
	v_mul_f32_e32 v53, 0x42800000, v53
	v_med3_f32 v56, v60, s50, v51
	v_med3_f32 v53, v53, s50, v51
	v_cvt_pk_fp8_f32 v52, v56, v53 op_sel:[0,0,1]
	s_waitcnt lgkmcnt(1)
	v_mul_f32_e32 v53, 0x42800000, v54
	v_mul_f32_e32 v54, 0x42800000, v55
	v_med3_f32 v56, v53, s50, v51
	v_med3_f32 v54, v54, s50, v51
	v_mov_b32_e32 v53, v3
	v_cvt_pk_fp8_f32 v53, v56, v54
	s_waitcnt lgkmcnt(0)
	v_mul_f32_e32 v55, 0x42800000, v58
	v_mul_f32_e32 v54, 0x42800000, v59
	v_med3_f32 v55, v55, s50, v51
	v_med3_f32 v54, v54, s50, v51
	v_cvt_pk_fp8_f32 v53, v55, v54 op_sel:[0,0,1]
	v_or_b32_e32 v54, s12, v15
	v_ashrrev_i32_e32 v55, 31, v54
	v_lshlrev_b64 v[54:55], 10, v[54:55]
	ds_read2_b32 v[56:57], v27 offset1:1
	v_lshl_add_u64 v[54:55], v[10:11], 0, v[54:55]
	global_store_dwordx2 v[54:55], v[52:53], off
	ds_read2_b32 v[52:53], v28 offset1:1
	ds_read2_b32 v[54:55], v29 offset1:1
	ds_read2_b32 v[58:59], v30 offset1:1
	s_waitcnt lgkmcnt(3)
	v_mul_f32_e32 v56, 0x42800000, v56
	v_mul_f32_e32 v57, 0x42800000, v57
	s_waitcnt lgkmcnt(2)
	v_mul_f32_e32 v60, 0x42800000, v52
	v_med3_f32 v56, v56, s50, v51
	v_med3_f32 v57, v57, s50, v51
	v_mov_b32_e32 v52, v3
	v_cvt_pk_fp8_f32 v52, v56, v57
	v_mul_f32_e32 v53, 0x42800000, v53
	v_med3_f32 v56, v60, s50, v51
	v_med3_f32 v53, v53, s50, v51
	v_cvt_pk_fp8_f32 v52, v56, v53 op_sel:[0,0,1]
	s_waitcnt lgkmcnt(1)
	v_mul_f32_e32 v53, 0x42800000, v54
	v_mul_f32_e32 v54, 0x42800000, v55
	v_med3_f32 v56, v53, s50, v51
	v_med3_f32 v54, v54, s50, v51
	v_mov_b32_e32 v53, v3
	v_cvt_pk_fp8_f32 v53, v56, v54
	s_waitcnt lgkmcnt(0)
	v_mul_f32_e32 v55, 0x42800000, v58
	v_mul_f32_e32 v54, 0x42800000, v59
	v_med3_f32 v55, v55, s50, v51
	v_med3_f32 v54, v54, s50, v51
	v_cvt_pk_fp8_f32 v53, v55, v54 op_sel:[0,0,1]
	v_or_b32_e32 v54, s12, v16
	v_ashrrev_i32_e32 v55, 31, v54
	v_lshlrev_b64 v[54:55], 10, v[54:55]
	ds_read2_b32 v[56:57], v31 offset1:1
	v_lshl_add_u64 v[54:55], v[10:11], 0, v[54:55]
	global_store_dwordx2 v[54:55], v[52:53], off
	ds_read2_b32 v[52:53], v32 offset1:1
	ds_read2_b32 v[54:55], v33 offset1:1
	ds_read2_b32 v[58:59], v34 offset1:1
	s_waitcnt lgkmcnt(3)
	v_mul_f32_e32 v56, 0x42800000, v56
	v_mul_f32_e32 v57, 0x42800000, v57
	s_waitcnt lgkmcnt(2)
	v_mul_f32_e32 v60, 0x42800000, v52
	v_med3_f32 v56, v56, s50, v51
	v_med3_f32 v57, v57, s50, v51
	v_mov_b32_e32 v52, v3
	v_cvt_pk_fp8_f32 v52, v56, v57
	v_mul_f32_e32 v53, 0x42800000, v53
	v_med3_f32 v56, v60, s50, v51
	v_med3_f32 v53, v53, s50, v51
	v_cvt_pk_fp8_f32 v52, v56, v53 op_sel:[0,0,1]
	s_waitcnt lgkmcnt(1)
	v_mul_f32_e32 v53, 0x42800000, v54
	v_mul_f32_e32 v54, 0x42800000, v55
	v_med3_f32 v56, v53, s50, v51
	v_med3_f32 v54, v54, s50, v51
	v_mov_b32_e32 v53, v3
	v_cvt_pk_fp8_f32 v53, v56, v54
	s_waitcnt lgkmcnt(0)
	v_mul_f32_e32 v55, 0x42800000, v58
	v_mul_f32_e32 v54, 0x42800000, v59
	v_med3_f32 v55, v55, s50, v51
	v_med3_f32 v54, v54, s50, v51
	v_cvt_pk_fp8_f32 v53, v55, v54 op_sel:[0,0,1]
	v_or_b32_e32 v54, s12, v17
	v_ashrrev_i32_e32 v55, 31, v54
	v_lshlrev_b64 v[54:55], 10, v[54:55]
	ds_read2_b32 v[56:57], v35 offset1:1
	v_lshl_add_u64 v[54:55], v[10:11], 0, v[54:55]
	global_store_dwordx2 v[54:55], v[52:53], off
	ds_read2_b32 v[52:53], v36 offset1:1
	ds_read2_b32 v[54:55], v37 offset1:1
	ds_read2_b32 v[58:59], v38 offset1:1
	s_waitcnt lgkmcnt(3)
	v_mul_f32_e32 v56, 0x42800000, v56
	v_mul_f32_e32 v57, 0x42800000, v57
	s_waitcnt lgkmcnt(2)
	v_mul_f32_e32 v60, 0x42800000, v52
	v_med3_f32 v56, v56, s50, v51
	v_med3_f32 v57, v57, s50, v51
	v_mov_b32_e32 v52, v3
	v_cvt_pk_fp8_f32 v52, v56, v57
	v_mul_f32_e32 v53, 0x42800000, v53
	v_med3_f32 v56, v60, s50, v51
	v_med3_f32 v53, v53, s50, v51
	v_cvt_pk_fp8_f32 v52, v56, v53 op_sel:[0,0,1]
	s_waitcnt lgkmcnt(1)
	v_mul_f32_e32 v53, 0x42800000, v54
	v_mul_f32_e32 v54, 0x42800000, v55
	v_med3_f32 v56, v53, s50, v51
	v_med3_f32 v54, v54, s50, v51
	v_mov_b32_e32 v53, v3
	v_cvt_pk_fp8_f32 v53, v56, v54
	s_waitcnt lgkmcnt(0)
	v_mul_f32_e32 v55, 0x42800000, v58
	v_mul_f32_e32 v54, 0x42800000, v59
	v_med3_f32 v55, v55, s50, v51
	v_med3_f32 v54, v54, s50, v51
	v_cvt_pk_fp8_f32 v53, v55, v54 op_sel:[0,0,1]
	v_or_b32_e32 v54, s12, v18
	v_ashrrev_i32_e32 v55, 31, v54
	v_lshlrev_b64 v[54:55], 10, v[54:55]
	ds_read2_b32 v[56:57], v39 offset1:1
	v_lshl_add_u64 v[54:55], v[10:11], 0, v[54:55]
	global_store_dwordx2 v[54:55], v[52:53], off
	ds_read2_b32 v[52:53], v40 offset1:1
	ds_read2_b32 v[54:55], v41 offset1:1
	ds_read2_b32 v[58:59], v42 offset1:1
	s_waitcnt lgkmcnt(3)
	v_mul_f32_e32 v56, 0x42800000, v56
	v_mul_f32_e32 v57, 0x42800000, v57
	s_waitcnt lgkmcnt(2)
	v_mul_f32_e32 v60, 0x42800000, v52
	v_med3_f32 v56, v56, s50, v51
	v_med3_f32 v57, v57, s50, v51
	v_mov_b32_e32 v52, v3
	v_cvt_pk_fp8_f32 v52, v56, v57
	v_mul_f32_e32 v53, 0x42800000, v53
	v_med3_f32 v56, v60, s50, v51
	v_med3_f32 v53, v53, s50, v51
	v_cvt_pk_fp8_f32 v52, v56, v53 op_sel:[0,0,1]
	s_waitcnt lgkmcnt(1)
	v_mul_f32_e32 v53, 0x42800000, v54
	v_mul_f32_e32 v54, 0x42800000, v55
	v_med3_f32 v56, v53, s50, v51
	v_med3_f32 v54, v54, s50, v51
	v_mov_b32_e32 v53, v3
	v_cvt_pk_fp8_f32 v53, v56, v54
	s_waitcnt lgkmcnt(0)
	v_mul_f32_e32 v55, 0x42800000, v58
	v_mul_f32_e32 v54, 0x42800000, v59
	v_med3_f32 v55, v55, s50, v51
	v_med3_f32 v54, v54, s50, v51
	v_cvt_pk_fp8_f32 v53, v55, v54 op_sel:[0,0,1]
	v_or_b32_e32 v54, s12, v19
	v_ashrrev_i32_e32 v55, 31, v54
	v_lshlrev_b64 v[54:55], 10, v[54:55]
	ds_read2_b32 v[56:57], v43 offset1:1
	v_lshl_add_u64 v[54:55], v[10:11], 0, v[54:55]
	global_store_dwordx2 v[54:55], v[52:53], off
	ds_read2_b32 v[52:53], v44 offset1:1
	ds_read2_b32 v[54:55], v45 offset1:1
	ds_read2_b32 v[58:59], v46 offset1:1
	s_waitcnt lgkmcnt(3)
	v_mul_f32_e32 v56, 0x42800000, v56
	v_mul_f32_e32 v57, 0x42800000, v57
	s_waitcnt lgkmcnt(2)
	v_mul_f32_e32 v60, 0x42800000, v52
	v_med3_f32 v56, v56, s50, v51
	v_med3_f32 v57, v57, s50, v51
	v_mov_b32_e32 v52, v3
	v_cvt_pk_fp8_f32 v52, v56, v57
	v_mul_f32_e32 v53, 0x42800000, v53
	v_med3_f32 v56, v60, s50, v51
	v_med3_f32 v53, v53, s50, v51
	v_cvt_pk_fp8_f32 v52, v56, v53 op_sel:[0,0,1]
	s_waitcnt lgkmcnt(1)
	v_mul_f32_e32 v53, 0x42800000, v54
	v_mul_f32_e32 v54, 0x42800000, v55
	v_med3_f32 v56, v53, s50, v51
	v_med3_f32 v54, v54, s50, v51
	v_mov_b32_e32 v53, v3
	v_cvt_pk_fp8_f32 v53, v56, v54
	s_waitcnt lgkmcnt(0)
	v_mul_f32_e32 v55, 0x42800000, v58
	v_mul_f32_e32 v54, 0x42800000, v59
	v_med3_f32 v55, v55, s50, v51
	v_med3_f32 v54, v54, s50, v51
	v_cvt_pk_fp8_f32 v53, v55, v54 op_sel:[0,0,1]
	v_or_b32_e32 v54, s12, v20
	v_ashrrev_i32_e32 v55, 31, v54
	v_lshlrev_b64 v[54:55], 10, v[54:55]
	ds_read2_b32 v[56:57], v47 offset1:1
	v_lshl_add_u64 v[54:55], v[10:11], 0, v[54:55]
	global_store_dwordx2 v[54:55], v[52:53], off
	ds_read2_b32 v[52:53], v48 offset1:1
	ds_read2_b32 v[54:55], v49 offset1:1
	ds_read2_b32 v[58:59], v50 offset1:1
	s_waitcnt lgkmcnt(3)
	v_mul_f32_e32 v56, 0x42800000, v56
	v_mul_f32_e32 v57, 0x42800000, v57
	s_waitcnt lgkmcnt(2)
	v_mul_f32_e32 v60, 0x42800000, v52
	v_med3_f32 v56, v56, s50, v51
	v_med3_f32 v57, v57, s50, v51
	v_mov_b32_e32 v52, v3
	v_cvt_pk_fp8_f32 v52, v56, v57
	v_mul_f32_e32 v53, 0x42800000, v53
	v_med3_f32 v56, v60, s50, v51
	v_med3_f32 v53, v53, s50, v51
	v_cvt_pk_fp8_f32 v52, v56, v53 op_sel:[0,0,1]
	s_waitcnt lgkmcnt(1)
	v_mul_f32_e32 v53, 0x42800000, v54
	v_mul_f32_e32 v54, 0x42800000, v55
	v_med3_f32 v56, v53, s50, v51
	v_med3_f32 v54, v54, s50, v51
	v_mov_b32_e32 v53, v3
	v_cvt_pk_fp8_f32 v53, v56, v54
	s_waitcnt lgkmcnt(0)
	v_mul_f32_e32 v55, 0x42800000, v58
	v_mul_f32_e32 v54, 0x42800000, v59
	v_med3_f32 v55, v55, s50, v51
	v_med3_f32 v54, v54, s50, v51
	v_cvt_pk_fp8_f32 v53, v55, v54 op_sel:[0,0,1]
	v_or_b32_e32 v54, s12, v21
	v_ashrrev_i32_e32 v55, 31, v54
	v_lshlrev_b64 v[54:55], 10, v[54:55]
	v_lshl_add_u64 v[10:11], v[10:11], 0, v[54:55]
	global_store_dwordx2 v[10:11], v[52:53], off
	s_waitcnt lgkmcnt(0)
	s_branch .LBB0_39
